# LayerNorm wave sums: DPP row reduction + row_bcast + readlane broadcast instead of six serialized ds_bpermute hops
# baseline (speedup 1.0000x reference)
; template <bool ROUTE, bool COMBINE> ...
;     ...
;         if (pre) {
; #pragma unroll
;             for (int j = 0; j < 4; ++j) bf8_to_f32(pre[j], v[2 * j], v[2 * j + 1]);
;         } else {
;             const bf16* yr = Yb + (size_t)row * D_ + 8 * lane;
; #pragma unroll
;             for (int j = 0; j < 4; ++j) bf8_to_f32(*(const u32x4*)(yr + 512 * j), v[2 * j], v[2 * j + 1]);
;         }
;     } else {
;         const int p0 = pos[row * 2], p1 = pos[row * 2 + 1]; const float g0 = topg[row * 2], g1 = topg[row * 2 + 1];
; #pragma unroll
;         for (int j = 0; j < 4; ++j) { const int c = 8 * lane + 512 * j;
;             f32x4 xa, xb, pa, pb, a0, a1, c0, c1;
;             bf8_to_f32(*(const u32x4*)(X1B + (size_t)row * D_ + c), xa, xb); bf8_to_f32(*(const u32x4*)(PLEB + (size_t)row * D_ + c), pa, pb);
;             bf8_to_f32(*(const u32x4*)(YE + (size_t)p0 * D_ + c), a0, a1);
;             bf8_to_f32(*(const u32x4*)(YE + (size_t)p1 * D_ + c), c0, c1);
;             v[2 * j] = (ALPHA * xa + (g0 * a0 + g1 * c0)) + pa; v[2 * j + 1] = (ALPHA * xb + (g0 * a1 + g1 * c1)) + pb; }
;     }
; #pragma unroll
;     for (int j = 0; j < 8; ++j) s += (v[j].x + v[j].y) + (v[j].z + v[j].w);
;     const float mean = wave_sum(s) * (1.0f / D_); float s2 = 0.f;
; #pragma unroll
;     for (int j = 0; j < 8; ++j) { v[j] = v[j] - mean; s2 += (v[j].x * v[j].x + v[j].y * v[j].y) + (v[j].z * v[j].z + v[j].w * v[j].w); }
;     const float rstd = 1.0f / sqrtf(wave_sum(s2) * (1.0f / D_) + LN_EPS);
.LBB0_633:
	s_waitcnt vmcnt(17)
	v_lshlrev_b32_e32 v119, 16, v88
	v_lshlrev_b32_e32 v118, 16, v90
	v_and_b32_e32 v121, 0xffff0000, v88
	v_and_b32_e32 v120, 0xffff0000, v90
	v_lshlrev_b32_e32 v115, 16, v89
	v_lshlrev_b32_e32 v114, 16, v91
	v_and_b32_e32 v117, 0xffff0000, v89
	v_and_b32_e32 v116, 0xffff0000, v91
	v_pk_add_f32 v[88:89], v[118:119], v[120:121]
	v_pk_add_f32 v[90:91], v[114:115], v[116:117]
	v_lshlrev_b32_e32 v102, 16, v81
	v_pk_add_f32 v[88:89], v[88:89], v[90:91]
	v_and_b32_e32 v106, 0xffff0000, v81
	v_add_f32_e32 v81, 0, v89
	v_add_f32_e32 v107, v88, v81
	v_lshlrev_b32_e32 v89, 16, v85
	v_lshlrev_b32_e32 v88, 16, v84
	v_and_b32_e32 v91, 0xffff0000, v85
	v_and_b32_e32 v90, 0xffff0000, v84
	v_pk_add_f32 v[84:85], v[88:89], v[90:91]
	v_lshlrev_b32_e32 v110, 16, v86
	v_and_b32_e32 v111, 0xffff0000, v86
	v_lshlrev_b32_e32 v112, 16, v87
	v_and_b32_e32 v113, 0xffff0000, v87
	v_pk_add_f32 v[84:85], v[84:85], v[84:85] op_sel_hi:[0,1]
	v_lshlrev_b32_e32 v104, 16, v80
	v_and_b32_e32 v108, 0xffff0000, v80
	v_add_f32_e32 v105, v110, v111
	v_add_f32_e32 v109, v112, v113
	v_mov_b32_e32 v103, v85
	v_pk_add_f32 v[130:131], v[104:105], v[108:109]
	v_pk_add_f32 v[84:85], v[102:103], v[106:107]
	s_waitcnt vmcnt(16)
	v_lshlrev_b32_e32 v98, 16, v92
	v_pk_add_f32 v[84:85], v[130:131], v[84:85]
	v_and_b32_e32 v99, 0xffff0000, v92
	v_pk_add_f32 v[130:131], v[84:85], v[84:85] op_sel_hi:[0,1]
	v_lshlrev_b32_e32 v85, 16, v83
	v_lshlrev_b32_e32 v84, 16, v82
	v_and_b32_e32 v83, 0xffff0000, v83
	v_and_b32_e32 v82, 0xffff0000, v82
	v_pk_add_f32 v[132:133], v[84:85], v[82:83]
	v_lshlrev_b32_e32 v100, 16, v93
	v_and_b32_e32 v101, 0xffff0000, v93
	v_pk_add_f32 v[132:133], v[132:133], v[132:133] op_sel_hi:[0,1]
	v_lshlrev_b32_e32 v86, 16, v94
	v_and_b32_e32 v94, 0xffff0000, v94
	v_lshlrev_b32_e32 v80, 16, v95
	v_and_b32_e32 v92, 0xffff0000, v95
	v_add_f32_e32 v87, v98, v99
	v_add_f32_e32 v95, v100, v101
	v_mov_b32_e32 v81, v133
	v_mov_b32_e32 v93, v131
	v_pk_add_f32 v[134:135], v[86:87], v[94:95]
	v_pk_add_f32 v[130:131], v[80:81], v[92:93]
	s_nop 0
	v_pk_add_f32 v[130:131], v[134:135], v[130:131]
	s_nop 0
	v_add_f32_e32 v81, v130, v131
	s_nop 1
	v_add_f32_dpp v81, v81, v81 quad_perm:[1,0,3,2] row_mask:0xf bank_mask:0xf
	s_nop 1
	v_add_f32_dpp v81, v81, v81 quad_perm:[2,3,0,1] row_mask:0xf bank_mask:0xf
	s_nop 1
	v_add_f32_dpp v81, v81, v81 row_half_mirror row_mask:0xf bank_mask:0xf
	s_nop 1
	v_add_f32_dpp v81, v81, v81 row_mirror row_mask:0xf bank_mask:0xf
	s_nop 1
	v_add_f32_dpp v81, v81, v81 row_bcast:15 row_mask:0xa bank_mask:0xf
	s_nop 1
	v_add_f32_dpp v81, v81, v81 row_bcast:31 row_mask:0xc bank_mask:0xf
	s_nop 1
	v_readlane_b32 s98, v81, 63
	s_nop 3
	v_mov_b32_e32 v81, s98
	s_waitcnt lgkmcnt(0)
	v_fmac_f32_e32 v121, 0xba000000, v81
	v_fmac_f32_e32 v120, 0xba000000, v81
	v_fmac_f32_e32 v117, 0xba000000, v81
	v_fmac_f32_e32 v119, 0xba000000, v81
	v_fmac_f32_e32 v116, 0xba000000, v81
	v_fmac_f32_e32 v118, 0xba000000, v81
	v_mov_b32_e32 v132, v121
	v_mov_b32_e32 v133, v120
	v_fmac_f32_e32 v115, 0xba000000, v81
	v_fmac_f32_e32 v114, 0xba000000, v81
	v_mov_b32_e32 v130, v119
	v_mov_b32_e32 v131, v118
	v_pk_mul_f32 v[132:133], v[132:133], v[132:133]
	v_mov_b32_e32 v134, v117
	v_mov_b32_e32 v135, v116
	v_pk_fma_f32 v[130:131], v[130:131], v[130:131], v[132:133]
	v_mov_b32_e32 v132, v115
	v_mov_b32_e32 v133, v114
	v_pk_mul_f32 v[134:135], v[134:135], v[134:135]
	v_fmac_f32_e32 v90, 0xba000000, v81
	v_pk_fma_f32 v[132:133], v[132:133], v[132:133], v[134:135]
	v_fmac_f32_e32 v91, 0xba000000, v81
	v_fmac_f32_e32 v89, 0xba000000, v81
	v_pk_add_f32 v[130:131], v[130:131], v[132:133]
	v_fmac_f32_e32 v88, 0xba000000, v81
	v_mov_b32_e32 v132, v89
	v_mov_b32_e32 v133, v91
	v_mov_b32_e32 v89, v90
	v_pk_mul_f32 v[134:135], v[132:133], v[132:133]
	v_pk_mul_f32 v[90:91], v[88:89], v[88:89]
	v_fmac_f32_e32 v110, 0xba000000, v81
	v_pk_mov_b32 v[136:137], v[90:91], v[134:135] op_sel:[1,0]
	v_mov_b32_e32 v91, v135
	v_pk_add_f32 v[90:91], v[136:137], v[90:91]
	v_fmac_f32_e32 v111, 0xba000000, v81
	v_pk_add_f32 v[90:91], v[90:91], v[90:91] op_sel_hi:[0,1]
	v_fmac_f32_e32 v112, 0xba000000, v81
	v_mul_f32_e32 v90, v110, v110
	v_fmac_f32_e32 v113, 0xba000000, v81
	v_pk_fma_f32 v[134:135], v[110:111], v[110:111], v[90:91] op_sel_hi:[1,1,0]
	v_mul_f32_e32 v90, v112, v112
	v_pk_add_f32 v[130:131], v[130:131], v[130:131] op_sel_hi:[0,1]
	v_pk_fma_f32 v[136:137], v[112:113], v[112:113], v[90:91] op_sel_hi:[1,1,0]
	v_fmac_f32_e32 v106, 0xba000000, v81
	v_fmac_f32_e32 v102, 0xba000000, v81
	v_fmac_f32_e32 v108, 0xba000000, v81
	v_fmac_f32_e32 v104, 0xba000000, v81
	v_mul_f32_e32 v134, v104, v104
	v_mul_f32_e32 v136, v108, v108
	v_mul_f32_e32 v90, v102, v102
	v_mul_f32_e32 v130, v106, v106
	v_fmac_f32_e32 v82, 0xba000000, v81
	v_fmac_f32_e32 v83, 0xba000000, v81
	v_fmac_f32_e32 v85, 0xba000000, v81
	v_pk_add_f32 v[134:135], v[134:135], v[136:137]
	v_pk_add_f32 v[90:91], v[90:91], v[130:131]
	v_fmac_f32_e32 v84, 0xba000000, v81
	v_mov_b32_e32 v130, v85
	v_mov_b32_e32 v131, v83
	v_mov_b32_e32 v85, v82
	v_pk_add_f32 v[90:91], v[134:135], v[90:91]
	v_pk_mul_f32 v[134:135], v[130:131], v[130:131]
	v_pk_mul_f32 v[82:83], v[84:85], v[84:85]
	v_fmac_f32_e32 v98, 0xba000000, v81
	v_pk_mov_b32 v[136:137], v[82:83], v[134:135] op_sel:[1,0]
	v_mov_b32_e32 v83, v135
	v_pk_add_f32 v[82:83], v[136:137], v[82:83]
	v_fmac_f32_e32 v99, 0xba000000, v81
	v_pk_add_f32 v[82:83], v[82:83], v[82:83] op_sel_hi:[0,1]
	v_fmac_f32_e32 v100, 0xba000000, v81
	v_mul_f32_e32 v82, v98, v98
	v_fmac_f32_e32 v101, 0xba000000, v81
	v_pk_fma_f32 v[134:135], v[98:99], v[98:99], v[82:83] op_sel_hi:[1,1,0]
	v_mul_f32_e32 v82, v100, v100
	v_pk_add_f32 v[90:91], v[90:91], v[90:91] op_sel_hi:[0,1]
	v_pk_fma_f32 v[136:137], v[100:101], v[100:101], v[82:83] op_sel_hi:[1,1,0]
	v_fmac_f32_e32 v92, 0xba000000, v81
	v_fmac_f32_e32 v80, 0xba000000, v81
	v_fmac_f32_e32 v94, 0xba000000, v81
	v_fmac_f32_e32 v86, 0xba000000, v81
	v_mul_f32_e32 v134, v86, v86
	v_mul_f32_e32 v136, v94, v94
	v_mul_f32_e32 v82, v80, v80
	v_mul_f32_e32 v90, v92, v92
	v_pk_add_f32 v[134:135], v[134:135], v[136:137]
	v_pk_add_f32 v[82:83], v[82:83], v[90:91]
	v_mov_b32_e32 v90, v114
	v_pk_add_f32 v[82:83], v[134:135], v[82:83]
	s_nop 0
	v_add_f32_e32 v81, v82, v83
	s_nop 1
	v_add_f32_dpp v81, v81, v81 quad_perm:[1,0,3,2] row_mask:0xf bank_mask:0xf
	s_nop 1
	v_add_f32_dpp v81, v81, v81 quad_perm:[2,3,0,1] row_mask:0xf bank_mask:0xf
	s_nop 1
	v_add_f32_dpp v81, v81, v81 row_half_mirror row_mask:0xf bank_mask:0xf
	s_nop 1
	v_add_f32_dpp v81, v81, v81 row_mirror row_mask:0xf bank_mask:0xf
	s_nop 1
	v_add_f32_dpp v81, v81, v81 row_bcast:15 row_mask:0xa bank_mask:0xf
	s_nop 1
	v_add_f32_dpp v81, v81, v81 row_bcast:31 row_mask:0xc bank_mask:0xf
	s_nop 1
	v_readlane_b32 s98, v81, 63
	s_nop 3
	v_mov_b32_e32 v81, s98
	v_mov_b32_e32 v83, v120
	v_mov_b32_e32 v120, v119
	s_waitcnt lgkmcnt(0)
; DI unsigned f2bf(float f) { unsigned u = __builtin_bit_cast(unsigned, f); return (u + 0x7fffu + ((u >> 16) & 1u)) >> 16; }
; template <bool ROUTE, bool COMBINE> ...
;     ...
;     const float rstd = 1.0f / sqrtf(wave_sum(s2) * (1.0f / D_) + LN_EPS);
;     float lg0 = 0.f, lg1 = 0.f, lg2 = 0.f, lg3 = 0.f, lg4 = 0.f, lg5 = 0.f, lg6 = 0.f, lg7 = 0.f;
; #pragma unroll
;     for (int j = 0; j < 4; ++j) {
;         const int c = 8 * lane + 512 * j;
;         const f32x4 oa = v[2 * j] * rstd * *(const f32x4*)(g + c) + *(const f32x4*)(bta + c), ob = v[2 * j + 1] * rstd * *(const f32x4*)(g + c + 4) + *(const f32x4*)(bta + c + 4);
;         if (X) { *(f32x4*)(X + (size_t)row * D_ + c) = oa; *(f32x4*)(X + (size_t)row * D_ + c + 4) = ob; }
;         if (XB) { u32x4 w; w.x = f2bf(oa.x) | (f2bf(oa.y) << 16); w.y = f2bf(oa.z) | (f2bf(oa.w) << 16); w.z = f2bf(ob.x) | (f2bf(ob.y) << 16); w.w = f2bf(ob.z) | (f2bf(ob.w) << 16);
;             *(u32x4*)(XB + (size_t)row * D_ + c) = w; }
	v_mov_b32_e32 v82, v118
	v_fmamk_f32 v81, v81, 0x3a000000, v128
	v_mul_f32_e32 v87, 0x4f800000, v81
	v_cmp_gt_f32_e32 vcc, s9, v81
	s_nop 1
	v_cndmask_b32_e32 v81, v81, v87, vcc
	v_sqrt_f32_e32 v87, v81
	s_nop 0
	v_add_u32_e32 v91, -1, v87
	v_fma_f32 v93, -v91, v87, v81
	v_cmp_ge_f32_e64 s[4:5], 0, v93
	v_add_u32_e32 v93, 1, v87
	s_nop 0
	v_cndmask_b32_e64 v91, v87, v91, s[4:5]
	v_fma_f32 v87, -v93, v87, v81
	v_cmp_lt_f32_e64 s[4:5], 0, v87
	s_nop 1
	v_cndmask_b32_e64 v87, v91, v93, s[4:5]
	v_mul_f32_e32 v91, 0x37800000, v87
	v_cndmask_b32_e32 v87, v87, v91, vcc
	v_cmp_class_f32_e32 vcc, v81, v129
	v_mov_b32_e32 v91, v116
	v_mov_b32_e32 v116, v115
	v_cndmask_b32_e32 v81, v87, v81, vcc
	v_div_scale_f32 v87, s[4:5], v81, v81, 1.0
	v_rcp_f32_e32 v93, v87
	s_nop 0
	v_fma_f32 v95, -v87, v93, 1.0
	v_fmac_f32_e32 v93, v95, v93
	v_div_scale_f32 v95, vcc, 1.0, v81, 1.0
	v_mul_f32_e32 v103, v95, v93
	v_fma_f32 v105, -v87, v103, v95
	v_fmac_f32_e32 v103, v105, v93
	v_fma_f32 v87, -v87, v103, v95
	v_div_fmas_f32 v87, v87, v93, v103
	v_div_fixup_f32 v118, v87, v81, 1.0
	v_pk_mul_f32 v[114:115], v[120:121], v[118:119] op_sel_hi:[1,0]
	v_pk_mul_f32 v[116:117], v[116:117], v[118:119] op_sel_hi:[1,0]
	s_waitcnt vmcnt(12)
	v_pk_fma_f32 v[114:115], v[4:5], v[114:115], v[12:13]
	v_pk_fma_f32 v[116:117], v[6:7], v[116:117], v[14:15]
	v_bfe_u32 v81, v114, 16, 1
	v_add3_u32 v81, v114, v81, s18
	v_bfe_u32 v87, v115, 16, 1
	v_lshrrev_b32_e32 v81, 16, v81
	v_add3_u32 v87, v115, v87, s18
	v_and_or_b32 v114, v87, s3, v81
	v_bfe_u32 v81, v116, 16, 1
	v_pk_mul_f32 v[82:83], v[82:83], v[118:119] op_sel_hi:[1,0]
	v_add3_u32 v81, v116, v81, s18
	v_bfe_u32 v87, v117, 16, 1
	v_pk_fma_f32 v[82:83], v[0:1], v[82:83], v[8:9]
	v_lshrrev_b32_e32 v81, 16, v81
	v_add3_u32 v87, v117, v87, s18
	v_and_or_b32 v115, v87, s3, v81
	v_bfe_u32 v81, v82, 16, 1
	v_pk_mul_f32 v[90:91], v[90:91], v[118:119] op_sel_hi:[1,0]
	v_add3_u32 v81, v82, v81, s18
	v_bfe_u32 v82, v83, 16, 1
	v_pk_fma_f32 v[90:91], v[2:3], v[90:91], v[10:11]
	v_lshrrev_b32_e32 v81, 16, v81
	v_add3_u32 v82, v83, v82, s18
	v_and_or_b32 v116, v82, s3, v81
	v_bfe_u32 v81, v90, 16, 1
	v_add3_u32 v81, v90, v81, s18
	v_bfe_u32 v82, v91, 16, 1
	v_lshrrev_b32_e32 v81, 16, v81
	v_add3_u32 v82, v91, v82, s18
	v_and_or_b32 v117, v82, s3, v81
	v_lshl_add_u64 v[82:83], s[10:11], 0, v[96:97]
	v_add_co_u32_e32 v120, vcc, s19, v82
	v_mov_b32_e32 v105, v108
	s_nop 0
	v_addc_co_u32_e32 v121, vcc, 0, v83, vcc
	v_pk_mul_f32 v[82:83], v[88:89], v[118:119] op_sel_hi:[1,0]
	v_pk_mul_f32 v[88:89], v[132:133], v[118:119] op_sel_hi:[1,0]
	s_waitcnt vmcnt(8)
	v_pk_fma_f32 v[82:83], v[20:21], v[82:83], v[28:29]
	v_pk_fma_f32 v[90:91], v[22:23], v[88:89], v[30:31]
	v_bfe_u32 v81, v82, 16, 1
	v_add3_u32 v81, v82, v81, s18
	v_bfe_u32 v82, v83, 16, 1
	v_pk_mul_f32 v[88:89], v[110:111], v[118:119] op_sel_hi:[1,0]
	v_lshrrev_b32_e32 v81, 16, v81
	v_add3_u32 v82, v83, v82, s18
	v_pk_mul_f32 v[110:111], v[112:113], v[118:119] op_sel_hi:[1,0]
	v_pk_fma_f32 v[112:113], v[16:17], v[88:89], v[24:25]
	v_and_or_b32 v88, v82, s3, v81
	v_bfe_u32 v81, v90, 16, 1
	v_add3_u32 v81, v90, v81, s18
	v_bfe_u32 v82, v91, 16, 1
	v_lshrrev_b32_e32 v81, 16, v81
	v_add3_u32 v82, v91, v82, s18
	v_and_or_b32 v89, v82, s3, v81
	v_bfe_u32 v81, v112, 16, 1
	v_add3_u32 v81, v112, v81, s18
	v_bfe_u32 v82, v113, 16, 1
	v_pk_fma_f32 v[110:111], v[18:19], v[110:111], v[26:27]
	v_lshrrev_b32_e32 v81, 16, v81
	v_add3_u32 v82, v113, v82, s18
	v_and_or_b32 v90, v82, s3, v81
	v_bfe_u32 v81, v110, 16, 1
	v_add3_u32 v81, v110, v81, s18
	v_bfe_u32 v82, v111, 16, 1
	v_lshrrev_b32_e32 v81, 16, v81
	v_add3_u32 v82, v111, v82, s18
	v_and_or_b32 v91, v82, s3, v81
	v_pk_mul_f32 v[82:83], v[104:105], v[118:119] op_sel_hi:[1,0]
	v_mov_b32_e32 v103, v106
	s_waitcnt vmcnt(4)
	v_pk_fma_f32 v[82:83], v[36:37], v[82:83], v[44:45]
	global_store_dwordx4 v[120:121], v[88:91], off offset:1024
	v_bfe_u32 v81, v82, 16, 1
	v_add3_u32 v81, v82, v81, s18
	v_pk_mul_f32 v[88:89], v[102:103], v[118:119] op_sel_hi:[1,0]
	v_bfe_u32 v82, v83, 16, 1
	v_pk_fma_f32 v[88:89], v[38:39], v[88:89], v[46:47]
	v_lshrrev_b32_e32 v81, 16, v81
	v_add3_u32 v82, v83, v82, s18
	v_and_or_b32 v82, v82, s3, v81
	v_bfe_u32 v81, v88, 16, 1
	v_pk_mul_f32 v[84:85], v[84:85], v[118:119] op_sel_hi:[1,0]
	v_add3_u32 v81, v88, v81, s18
	v_bfe_u32 v83, v89, 16, 1
	v_pk_fma_f32 v[84:85], v[32:33], v[84:85], v[40:41]
	v_lshrrev_b32_e32 v81, 16, v81
	v_add3_u32 v83, v89, v83, s18
	v_and_or_b32 v83, v83, s3, v81
	v_bfe_u32 v81, v84, 16, 1
	v_pk_mul_f32 v[90:91], v[130:131], v[118:119] op_sel_hi:[1,0]
	v_add3_u32 v81, v84, v81, s18
	v_bfe_u32 v84, v85, 16, 1
	v_pk_fma_f32 v[90:91], v[34:35], v[90:91], v[42:43]
	v_lshrrev_b32_e32 v81, 16, v81
	v_add3_u32 v84, v85, v84, s18
	v_and_or_b32 v84, v84, s3, v81
	v_bfe_u32 v81, v90, 16, 1
	v_add3_u32 v81, v90, v81, s18
	v_bfe_u32 v85, v91, 16, 1
	v_lshrrev_b32_e32 v81, 16, v81
	v_add3_u32 v85, v91, v85, s18
	v_and_or_b32 v85, v85, s3, v81
	global_store_dwordx4 v[120:121], v[82:85], off offset:2048
	v_mov_b32_e32 v81, v92
	v_pk_mul_f32 v[80:81], v[80:81], v[118:119] op_sel_hi:[1,0]
	v_pk_mul_f32 v[82:83], v[98:99], v[118:119] op_sel_hi:[1,0]
	s_waitcnt vmcnt(3)
	v_pk_fma_f32 v[88:89], v[50:51], v[80:81], v[58:59]
	s_waitcnt vmcnt(2)
	v_pk_fma_f32 v[82:83], v[52:53], v[82:83], v[60:61]
	v_pk_mul_f32 v[84:85], v[100:101], v[118:119] op_sel_hi:[1,0]
	v_bfe_u32 v80, v82, 16, 1
	v_add3_u32 v80, v82, v80, s18
	v_bfe_u32 v81, v83, 16, 1
	v_pk_fma_f32 v[84:85], v[54:55], v[84:85], v[62:63]
	v_lshrrev_b32_e32 v80, 16, v80
	v_add3_u32 v81, v83, v81, s18
	v_mov_b32_e32 v87, v94
	v_and_or_b32 v80, v81, s3, v80
	v_bfe_u32 v81, v84, 16, 1
	v_pk_mul_f32 v[86:87], v[86:87], v[118:119] op_sel_hi:[1,0]
	v_add3_u32 v81, v84, v81, s18
	v_bfe_u32 v82, v85, 16, 1
	v_pk_fma_f32 v[86:87], v[48:49], v[86:87], v[56:57]
	v_lshrrev_b32_e32 v81, 16, v81
	v_add3_u32 v82, v85, v82, s18
	v_and_or_b32 v81, v82, s3, v81
	v_bfe_u32 v82, v86, 16, 1
	v_add3_u32 v82, v86, v82, s18
	v_bfe_u32 v83, v87, 16, 1
	v_lshrrev_b32_e32 v82, 16, v82
	v_add3_u32 v83, v87, v83, s18
	v_and_or_b32 v82, v83, s3, v82
	v_bfe_u32 v83, v88, 16, 1
	v_add3_u32 v83, v88, v83, s18
	v_bfe_u32 v84, v89, 16, 1
	s_add_u32 s10, s10, s12
	v_lshrrev_b32_e32 v83, 16, v83
	v_add3_u32 v84, v89, v84, s18
	s_addc_u32 s11, s11, s13
	v_and_or_b32 v83, v84, s3, v83
	s_add_u32 s14, s14, s12
	global_store_dwordx4 v[120:121], v[80:83], off offset:3072
	s_addc_u32 s15, s15, s13
	s_andn2_b64 vcc, exec, s[16:17]
	v_mov_b32_e32 v92, v76
	v_mov_b32_e32 v93, v77
	v_mov_b32_e32 v94, v78
	v_mov_b32_e32 v95, v79
	v_mov_b32_e32 v80, v72
	v_mov_b32_e32 v81, v73
	v_mov_b32_e32 v82, v74
	v_mov_b32_e32 v83, v75
	v_mov_b32_e32 v84, v68
	v_mov_b32_e32 v85, v69
	v_mov_b32_e32 v86, v70
	v_mov_b32_e32 v87, v71
	v_mov_b32_e32 v88, v64
	v_mov_b32_e32 v89, v65
	v_mov_b32_e32 v90, v66
	v_mov_b32_e32 v91, v67
	global_store_dwordx4 v[120:121], v[114:117], off
	s_cbranch_vccz .LBB0_636

; template <bool ROUTE, bool COMBINE> ...
;     ...
;         if (pre) {
; #pragma unroll
;             for (int j = 0; j < 4; ++j) bf8_to_f32(pre[j], v[2 * j], v[2 * j + 1]);
;         } else {
;             const bf16* yr = Yb + (size_t)row * D_ + 8 * lane;
; #pragma unroll
;             for (int j = 0; j < 4; ++j) bf8_to_f32(*(const u32x4*)(yr + 512 * j), v[2 * j], v[2 * j + 1]);
;         }
;     } else {
;         const int p0 = pos[row * 2], p1 = pos[row * 2 + 1]; const float g0 = topg[row * 2], g1 = topg[row * 2 + 1];
; #pragma unroll
;         for (int j = 0; j < 4; ++j) { const int c = 8 * lane + 512 * j;
;             f32x4 xa, xb, pa, pb, a0, a1, c0, c1;
;             bf8_to_f32(*(const u32x4*)(X1B + (size_t)row * D_ + c), xa, xb); bf8_to_f32(*(const u32x4*)(PLEB + (size_t)row * D_ + c), pa, pb);
;             bf8_to_f32(*(const u32x4*)(YE + (size_t)p0 * D_ + c), a0, a1);
;             bf8_to_f32(*(const u32x4*)(YE + (size_t)p1 * D_ + c), c0, c1);
;             v[2 * j] = (ALPHA * xa + (g0 * a0 + g1 * c0)) + pa; v[2 * j + 1] = (ALPHA * xb + (g0 * a1 + g1 * c1)) + pb; }
;     }
; #pragma unroll
;     for (int j = 0; j < 8; ++j) s += (v[j].x + v[j].y) + (v[j].z + v[j].w);
;     const float mean = wave_sum(s) * (1.0f / D_); float s2 = 0.f;
; #pragma unroll
;     for (int j = 0; j < 8; ++j) { v[j] = v[j] - mean; s2 += (v[j].x * v[j].x + v[j].y * v[j].y) + (v[j].z * v[j].z + v[j].w * v[j].w); }
;     const float rstd = 1.0f / sqrtf(wave_sum(s2) * (1.0f / D_) + LN_EPS);
.LBB0_873:
	s_waitcnt vmcnt(17)
	v_lshlrev_b32_e32 v123, 16, v88
	v_lshlrev_b32_e32 v122, 16, v90
	v_and_b32_e32 v125, 0xffff0000, v88
	v_and_b32_e32 v124, 0xffff0000, v90
	v_lshlrev_b32_e32 v119, 16, v89
	v_lshlrev_b32_e32 v118, 16, v91
	v_and_b32_e32 v121, 0xffff0000, v89
	v_and_b32_e32 v120, 0xffff0000, v91
	v_pk_add_f32 v[88:89], v[122:123], v[124:125]
	v_pk_add_f32 v[90:91], v[118:119], v[120:121]
	v_lshlrev_b32_e32 v106, 16, v81
	v_pk_add_f32 v[88:89], v[88:89], v[90:91]
	v_and_b32_e32 v110, 0xffff0000, v81
	v_add_f32_e32 v81, 0, v89
	v_add_f32_e32 v111, v88, v81
	v_lshlrev_b32_e32 v89, 16, v85
	v_lshlrev_b32_e32 v88, 16, v84
	v_and_b32_e32 v91, 0xffff0000, v85
	v_and_b32_e32 v90, 0xffff0000, v84
	v_pk_add_f32 v[84:85], v[88:89], v[90:91]
	v_lshlrev_b32_e32 v114, 16, v86
	v_and_b32_e32 v115, 0xffff0000, v86
	v_lshlrev_b32_e32 v116, 16, v87
	v_and_b32_e32 v117, 0xffff0000, v87
	v_pk_add_f32 v[84:85], v[84:85], v[84:85] op_sel_hi:[0,1]
	v_lshlrev_b32_e32 v108, 16, v80
	v_and_b32_e32 v112, 0xffff0000, v80
	v_add_f32_e32 v109, v114, v115
	v_add_f32_e32 v113, v116, v117
	v_mov_b32_e32 v107, v85
	v_pk_add_f32 v[136:137], v[108:109], v[112:113]
	v_pk_add_f32 v[84:85], v[106:107], v[110:111]
	v_and_b32_e32 v139, 0xffff0000, v83
	v_pk_add_f32 v[84:85], v[136:137], v[84:85]
	v_and_b32_e32 v138, 0xffff0000, v82
	v_pk_add_f32 v[136:137], v[84:85], v[84:85] op_sel_hi:[0,1]
	v_lshlrev_b32_e32 v85, 16, v83
	v_lshlrev_b32_e32 v84, 16, v82
	v_pk_add_f32 v[82:83], v[84:85], v[138:139]
	s_waitcnt vmcnt(16)
	v_lshlrev_b32_e32 v102, 16, v92
	v_and_b32_e32 v103, 0xffff0000, v92
	v_lshlrev_b32_e32 v104, 16, v93
	v_and_b32_e32 v105, 0xffff0000, v93
	v_pk_add_f32 v[82:83], v[82:83], v[82:83] op_sel_hi:[0,1]
	v_lshlrev_b32_e32 v86, 16, v94
	v_and_b32_e32 v94, 0xffff0000, v94
	v_lshlrev_b32_e32 v80, 16, v95
	v_and_b32_e32 v92, 0xffff0000, v95
	v_add_f32_e32 v87, v102, v103
	v_add_f32_e32 v95, v104, v105
	v_mov_b32_e32 v81, v83
	v_mov_b32_e32 v93, v137
	v_pk_add_f32 v[140:141], v[86:87], v[94:95]
	v_pk_add_f32 v[82:83], v[80:81], v[92:93]
	v_lshl_add_u64 v[100:101], v[100:101], 0, s[14:15]
	v_pk_add_f32 v[82:83], v[140:141], v[82:83]
	s_nop 0
	v_add_f32_e32 v81, v82, v83
	s_nop 1
	v_add_f32_dpp v81, v81, v81 quad_perm:[1,0,3,2] row_mask:0xf bank_mask:0xf
	s_nop 1
	v_add_f32_dpp v81, v81, v81 quad_perm:[2,3,0,1] row_mask:0xf bank_mask:0xf
	s_nop 1
	v_add_f32_dpp v81, v81, v81 row_half_mirror row_mask:0xf bank_mask:0xf
	s_nop 1
	v_add_f32_dpp v81, v81, v81 row_mirror row_mask:0xf bank_mask:0xf
	s_nop 1
	v_add_f32_dpp v81, v81, v81 row_bcast:15 row_mask:0xa bank_mask:0xf
	s_nop 1
	v_add_f32_dpp v81, v81, v81 row_bcast:31 row_mask:0xc bank_mask:0xf
	s_nop 1
	v_readlane_b32 s98, v81, 63
	s_nop 3
	v_mov_b32_e32 v81, s98
	s_waitcnt lgkmcnt(0)
	v_fmac_f32_e32 v125, 0xba000000, v81
	v_fmac_f32_e32 v124, 0xba000000, v81
	v_fmac_f32_e32 v121, 0xba000000, v81
	v_fmac_f32_e32 v123, 0xba000000, v81
	v_fmac_f32_e32 v120, 0xba000000, v81
	v_fmac_f32_e32 v122, 0xba000000, v81
	v_mov_b32_e32 v136, v125
	v_mov_b32_e32 v137, v124
	v_fmac_f32_e32 v119, 0xba000000, v81
	v_fmac_f32_e32 v118, 0xba000000, v81
	v_mov_b32_e32 v82, v123
	v_mov_b32_e32 v83, v122
	v_pk_mul_f32 v[136:137], v[136:137], v[136:137]
	v_mov_b32_e32 v140, v121
	v_mov_b32_e32 v141, v120
	v_pk_fma_f32 v[82:83], v[82:83], v[82:83], v[136:137]
	v_mov_b32_e32 v136, v119
	v_mov_b32_e32 v137, v118
	v_pk_mul_f32 v[140:141], v[140:141], v[140:141]
	v_fmac_f32_e32 v90, 0xba000000, v81
	v_pk_fma_f32 v[136:137], v[136:137], v[136:137], v[140:141]
	v_fmac_f32_e32 v91, 0xba000000, v81
	v_fmac_f32_e32 v89, 0xba000000, v81
	v_pk_add_f32 v[82:83], v[82:83], v[136:137]
	v_fmac_f32_e32 v88, 0xba000000, v81
	v_mov_b32_e32 v136, v89
	v_mov_b32_e32 v137, v91
	v_mov_b32_e32 v89, v90
	v_pk_add_f32 v[82:83], v[82:83], v[82:83] op_sel_hi:[0,1]
	v_pk_mul_f32 v[140:141], v[136:137], v[136:137]
	v_pk_mul_f32 v[90:91], v[88:89], v[88:89]
	v_fmac_f32_e32 v114, 0xba000000, v81
	v_pk_mov_b32 v[142:143], v[90:91], v[140:141] op_sel:[1,0]
	v_mov_b32_e32 v91, v141
	v_fmac_f32_e32 v115, 0xba000000, v81
	v_fmac_f32_e32 v116, 0xba000000, v81
	v_mul_f32_e32 v82, v114, v114
	v_pk_add_f32 v[90:91], v[142:143], v[90:91]
	v_fmac_f32_e32 v117, 0xba000000, v81
	v_pk_fma_f32 v[140:141], v[114:115], v[114:115], v[82:83] op_sel_hi:[1,1,0]
	v_mul_f32_e32 v82, v116, v116
	v_pk_add_f32 v[90:91], v[90:91], v[90:91] op_sel_hi:[0,1]
	v_pk_fma_f32 v[142:143], v[116:117], v[116:117], v[82:83] op_sel_hi:[1,1,0]
	v_fmac_f32_e32 v110, 0xba000000, v81
	v_fmac_f32_e32 v106, 0xba000000, v81
	v_fmac_f32_e32 v112, 0xba000000, v81
	v_fmac_f32_e32 v108, 0xba000000, v81
	v_mul_f32_e32 v140, v108, v108
	v_mul_f32_e32 v142, v112, v112
	v_mul_f32_e32 v90, v106, v106
	v_mul_f32_e32 v82, v110, v110
	v_pk_add_f32 v[140:141], v[140:141], v[142:143]
	v_pk_add_f32 v[82:83], v[90:91], v[82:83]
	v_fmac_f32_e32 v138, 0xba000000, v81
	v_pk_add_f32 v[82:83], v[140:141], v[82:83]
	v_fmac_f32_e32 v139, 0xba000000, v81
	v_fmac_f32_e32 v85, 0xba000000, v81
	v_pk_add_f32 v[90:91], v[82:83], v[82:83] op_sel_hi:[0,1]
	v_fmac_f32_e32 v84, 0xba000000, v81
	v_mov_b32_e32 v82, v85
	v_mov_b32_e32 v83, v139
	v_mov_b32_e32 v85, v138
	v_pk_mul_f32 v[140:141], v[82:83], v[82:83]
	v_pk_mul_f32 v[138:139], v[84:85], v[84:85]
	v_fmac_f32_e32 v102, 0xba000000, v81
	v_pk_mov_b32 v[142:143], v[138:139], v[140:141] op_sel:[1,0]
	v_mov_b32_e32 v139, v141
	v_fmac_f32_e32 v103, 0xba000000, v81
	v_fmac_f32_e32 v104, 0xba000000, v81
	v_mul_f32_e32 v90, v102, v102
	v_pk_add_f32 v[138:139], v[142:143], v[138:139]
	v_fmac_f32_e32 v105, 0xba000000, v81
	v_pk_fma_f32 v[140:141], v[102:103], v[102:103], v[90:91] op_sel_hi:[1,1,0]
	v_mul_f32_e32 v90, v104, v104
	v_pk_add_f32 v[138:139], v[138:139], v[138:139] op_sel_hi:[0,1]
	v_pk_fma_f32 v[142:143], v[104:105], v[104:105], v[90:91] op_sel_hi:[1,1,0]
	v_fmac_f32_e32 v92, 0xba000000, v81
	v_fmac_f32_e32 v80, 0xba000000, v81
	v_fmac_f32_e32 v94, 0xba000000, v81
	v_fmac_f32_e32 v86, 0xba000000, v81
	v_mul_f32_e32 v140, v86, v86
	v_mul_f32_e32 v142, v94, v94
	v_mul_f32_e32 v138, v80, v80
	v_mul_f32_e32 v90, v92, v92
	v_pk_add_f32 v[140:141], v[140:141], v[142:143]
	v_pk_add_f32 v[90:91], v[138:139], v[90:91]
	v_lshl_add_u64 v[142:143], s[10:11], 0, v[98:99]
	v_pk_add_f32 v[90:91], v[140:141], v[90:91]
	v_lshl_add_u64 v[98:99], v[98:99], 0, s[14:15]
	v_add_f32_e32 v81, v90, v91
	s_nop 1
	v_add_f32_dpp v81, v81, v81 quad_perm:[1,0,3,2] row_mask:0xf bank_mask:0xf
	s_nop 1
	v_add_f32_dpp v81, v81, v81 quad_perm:[2,3,0,1] row_mask:0xf bank_mask:0xf
	s_nop 1
	v_add_f32_dpp v81, v81, v81 row_half_mirror row_mask:0xf bank_mask:0xf
	s_nop 1
	v_add_f32_dpp v81, v81, v81 row_mirror row_mask:0xf bank_mask:0xf
	s_nop 1
	v_add_f32_dpp v81, v81, v81 row_bcast:15 row_mask:0xa bank_mask:0xf
	s_nop 1
	v_add_f32_dpp v81, v81, v81 row_bcast:31 row_mask:0xc bank_mask:0xf
	s_nop 1
	v_readlane_b32 s98, v81, 63
	s_nop 3
	v_mov_b32_e32 v81, s98
	v_mov_b32_e32 v91, v124
	v_mov_b32_e32 v124, v123
	v_mov_b32_e32 v90, v122
	v_mov_b32_e32 v122, v118
	s_waitcnt lgkmcnt(0)
; DI unsigned f2bf(float f) { unsigned u = __builtin_bit_cast(unsigned, f); return (u + 0x7fffu + ((u >> 16) & 1u)) >> 16; }
; template <bool ROUTE, bool COMBINE> ...
;     ...
;     const float rstd = 1.0f / sqrtf(wave_sum(s2) * (1.0f / D_) + LN_EPS);
;     float lg0 = 0.f, lg1 = 0.f, lg2 = 0.f, lg3 = 0.f, lg4 = 0.f, lg5 = 0.f, lg6 = 0.f, lg7 = 0.f;
; #pragma unroll
;     for (int j = 0; j < 4; ++j) {
;         const int c = 8 * lane + 512 * j;
;         const f32x4 oa = v[2 * j] * rstd * *(const f32x4*)(g + c) + *(const f32x4*)(bta + c), ob = v[2 * j + 1] * rstd * *(const f32x4*)(g + c + 4) + *(const f32x4*)(bta + c + 4);
;         if (X) { *(f32x4*)(X + (size_t)row * D_ + c) = oa; *(f32x4*)(X + (size_t)row * D_ + c + 4) = ob; }
;         if (XB) { u32x4 w; w.x = f2bf(oa.x) | (f2bf(oa.y) << 16); w.y = f2bf(oa.z) | (f2bf(oa.w) << 16); w.z = f2bf(ob.x) | (f2bf(ob.y) << 16); w.w = f2bf(ob.z) | (f2bf(ob.w) << 16);
;             *(u32x4*)(XB + (size_t)row * D_ + c) = w; }
;         if (XB8) { const f32x4 sa = oa * 16.f, sb = ob * 16.f;
;             int w0 = __builtin_amdgcn_cvt_pk_fp8_f32(__builtin_amdgcn_fmed3f(sa.x, -448.f, 448.f), __builtin_amdgcn_fmed3f(sa.y, -448.f, 448.f), 0, false);
;             w0 = __builtin_amdgcn_cvt_pk_fp8_f32(__builtin_amdgcn_fmed3f(sa.z, -448.f, 448.f), __builtin_amdgcn_fmed3f(sa.w, -448.f, 448.f), w0, true);
;             int w1 = __builtin_amdgcn_cvt_pk_fp8_f32(__builtin_amdgcn_fmed3f(sb.x, -448.f, 448.f), __builtin_amdgcn_fmed3f(sb.y, -448.f, 448.f), 0, false);
;             w1 = __builtin_amdgcn_cvt_pk_fp8_f32(__builtin_amdgcn_fmed3f(sb.z, -448.f, 448.f), __builtin_amdgcn_fmed3f(sb.w, -448.f, 448.f), w1, true);
;             *(u32x2*)(XB8 + (size_t)row * D_ + c) = (u32x2){(unsigned)w0, (unsigned)w1}; }
	v_mov_b32_e32 v123, v120
	v_mov_b32_e32 v120, v119
	v_fmamk_f32 v81, v81, 0x3a000000, v132
	v_mul_f32_e32 v87, 0x4f800000, v81
	v_cmp_gt_f32_e32 vcc, s9, v81
	s_nop 1
	v_cndmask_b32_e32 v81, v81, v87, vcc
	v_sqrt_f32_e32 v87, v81
	s_nop 0
	v_add_u32_e32 v93, -1, v87
	v_fma_f32 v95, -v93, v87, v81
	v_cmp_ge_f32_e64 s[4:5], 0, v95
	v_add_u32_e32 v95, 1, v87
	s_nop 0
	v_cndmask_b32_e64 v93, v87, v93, s[4:5]
	v_fma_f32 v87, -v95, v87, v81
	v_cmp_lt_f32_e64 s[4:5], 0, v87
	s_nop 1
	v_cndmask_b32_e64 v87, v93, v95, s[4:5]
	v_mul_f32_e32 v93, 0x37800000, v87
	v_cndmask_b32_e32 v87, v87, v93, vcc
	v_cmp_class_f32_e32 vcc, v81, v133
	s_nop 1
	v_cndmask_b32_e32 v81, v87, v81, vcc
	v_div_scale_f32 v87, s[4:5], v81, v81, 1.0
	v_rcp_f32_e32 v93, v87
	s_nop 0
	v_fma_f32 v95, -v87, v93, 1.0
	v_fmac_f32_e32 v93, v95, v93
	v_div_scale_f32 v95, vcc, 1.0, v81, 1.0
	v_mul_f32_e32 v107, v95, v93
	v_fma_f32 v109, -v87, v107, v95
	v_fmac_f32_e32 v107, v109, v93
	v_fma_f32 v87, -v87, v107, v95
	v_div_fmas_f32 v87, v87, v93, v107
	v_div_fixup_f32 v138, v87, v81, 1.0
	v_pk_mul_f32 v[118:119], v[124:125], v[138:139] op_sel_hi:[1,0]
	v_pk_mul_f32 v[120:121], v[120:121], v[138:139] op_sel_hi:[1,0]
	s_waitcnt vmcnt(12)
	v_pk_fma_f32 v[140:141], v[8:9], v[118:119], v[16:17]
	v_pk_fma_f32 v[124:125], v[10:11], v[120:121], v[18:19]
	v_bfe_u32 v81, v140, 16, 1
	v_add3_u32 v81, v140, v81, s17
	v_bfe_u32 v87, v141, 16, 1
	v_pk_mul_f32 v[118:119], v[122:123], v[138:139] op_sel_hi:[1,0]
	v_lshrrev_b32_e32 v81, 16, v81
	v_add3_u32 v87, v141, v87, s17
	v_pk_fma_f32 v[122:123], v[6:7], v[118:119], v[14:15]
	v_and_or_b32 v118, v87, s3, v81
	v_bfe_u32 v81, v124, 16, 1
	v_pk_mul_f32 v[90:91], v[90:91], v[138:139] op_sel_hi:[1,0]
	v_add3_u32 v81, v124, v81, s17
	v_bfe_u32 v87, v125, 16, 1
	v_pk_fma_f32 v[90:91], v[4:5], v[90:91], v[12:13]
	v_lshrrev_b32_e32 v81, 16, v81
	v_add3_u32 v87, v125, v87, s17
	v_and_or_b32 v119, v87, s3, v81
	v_bfe_u32 v81, v90, 16, 1
	v_add3_u32 v81, v90, v81, s17
	v_bfe_u32 v87, v91, 16, 1
	v_lshrrev_b32_e32 v81, 16, v81
	v_add3_u32 v87, v91, v87, s17
	v_and_or_b32 v120, v87, s3, v81
	v_bfe_u32 v81, v122, 16, 1
	v_add3_u32 v81, v122, v81, s17
	v_bfe_u32 v87, v123, 16, 1
	v_lshrrev_b32_e32 v81, 16, v81
	v_add3_u32 v87, v123, v87, s17
	v_add_co_u32_e32 v142, vcc, s20, v142
	v_and_or_b32 v121, v87, s3, v81
	s_nop 0
	v_addc_co_u32_e32 v143, vcc, 0, v143, vcc
	global_store_dwordx4 v[142:143], v[118:121], off
	v_pk_mul_f32 v[90:91], v[90:91], s[16:17] op_sel_hi:[1,0]
	v_pk_mul_f32 v[122:123], v[122:123], s[16:17] op_sel_hi:[1,0]
	v_pk_mul_f32 v[120:121], v[140:141], s[16:17] op_sel_hi:[1,0]
	v_med3_f32 v90, v90, s21, v134
	v_med3_f32 v81, v120, s21, v134
	v_med3_f32 v87, v121, s21, v134
	v_mov_b32_e32 v120, 0
	v_cvt_pk_fp8_f32 v120, v81, v87
	v_med3_f32 v91, v91, s21, v134
	v_mov_b32_e32 v121, 0
	v_cvt_pk_fp8_f32 v121, v90, v91
	v_pk_mul_f32 v[118:119], v[124:125], s[16:17] op_sel_hi:[1,0]
	v_pk_mul_f32 v[88:89], v[88:89], v[138:139] op_sel_hi:[1,0]
	v_med3_f32 v81, v118, s21, v134
	v_med3_f32 v87, v119, s21, v134
	v_cvt_pk_fp8_f32 v120, v81, v87 op_sel:[0,0,1]
	v_med3_f32 v81, v122, s21, v134
	v_med3_f32 v87, v123, s21, v134
	v_cvt_pk_fp8_f32 v121, v81, v87 op_sel:[0,0,1]
	v_lshl_add_u64 v[90:91], s[10:11], 0, v[96:97]
	s_waitcnt vmcnt(9)
	v_pk_fma_f32 v[122:123], v[24:25], v[88:89], v[32:33]
	v_add_co_u32_e32 v118, vcc, s22, v90
	v_bfe_u32 v81, v122, 16, 1
	s_nop 0
	v_addc_co_u32_e32 v119, vcc, 0, v91, vcc
	v_pk_mul_f32 v[90:91], v[136:137], v[138:139] op_sel_hi:[1,0]
	v_add3_u32 v81, v122, v81, s17
	v_bfe_u32 v87, v123, 16, 1
	global_store_dwordx2 v[118:119], v[120:121], off
	v_pk_fma_f32 v[120:121], v[26:27], v[90:91], v[34:35]
	v_pk_mul_f32 v[88:89], v[114:115], v[138:139] op_sel_hi:[1,0]
	v_lshrrev_b32_e32 v81, 16, v81
	v_add3_u32 v87, v123, v87, s17
	v_pk_mul_f32 v[90:91], v[116:117], v[138:139] op_sel_hi:[1,0]
	v_pk_fma_f32 v[116:117], v[20:21], v[88:89], v[28:29]
	v_and_or_b32 v88, v87, s3, v81
	v_bfe_u32 v81, v120, 16, 1
	v_add3_u32 v81, v120, v81, s17
	v_bfe_u32 v87, v121, 16, 1
	v_lshrrev_b32_e32 v81, 16, v81
	v_add3_u32 v87, v121, v87, s17
	v_and_or_b32 v89, v87, s3, v81
	v_bfe_u32 v81, v116, 16, 1
	v_bfe_u32 v87, v117, 16, 1
	v_pk_mul_f32 v[122:123], v[122:123], s[16:17] op_sel_hi:[1,0]
	v_pk_fma_f32 v[114:115], v[22:23], v[90:91], v[30:31]
	v_add3_u32 v81, v116, v81, s17
	v_add3_u32 v87, v117, v87, s17
	v_pk_mul_f32 v[116:117], v[116:117], s[16:17] op_sel_hi:[1,0]
	v_med3_f32 v91, v122, s21, v134
	v_med3_f32 v93, v123, s21, v134
	v_mov_b32_e32 v122, 0
	v_cvt_pk_fp8_f32 v122, v91, v93
	v_med3_f32 v95, v116, s21, v134
	v_med3_f32 v107, v117, s21, v134
	v_mov_b32_e32 v123, 0
	v_cvt_pk_fp8_f32 v123, v95, v107
	v_pk_mul_f32 v[120:121], v[120:121], s[16:17] op_sel_hi:[1,0]
	v_lshrrev_b32_e32 v81, 16, v81
	v_pk_mul_f32 v[124:125], v[114:115], s[16:17] op_sel_hi:[1,0]
	v_med3_f32 v91, v120, s21, v134
	v_med3_f32 v93, v121, s21, v134
	v_and_or_b32 v90, v87, s3, v81
	v_bfe_u32 v81, v114, 16, 1
	v_cvt_pk_fp8_f32 v122, v91, v93 op_sel:[0,0,1]
	v_med3_f32 v91, v124, s21, v134
	v_med3_f32 v93, v125, s21, v134
	v_add3_u32 v81, v114, v81, s17
	v_bfe_u32 v87, v115, 16, 1
	v_cvt_pk_fp8_f32 v123, v91, v93 op_sel:[0,0,1]
	v_lshrrev_b32_e32 v81, 16, v81
	v_add3_u32 v87, v115, v87, s17
	v_and_or_b32 v91, v87, s3, v81
	v_mov_b32_e32 v109, v112
	global_store_dwordx4 v[142:143], v[88:91], off offset:1024
	global_store_dwordx2 v[118:119], v[122:123], off offset:512
	v_mov_b32_e32 v107, v110
	v_pk_mul_f32 v[88:89], v[108:109], v[138:139] op_sel_hi:[1,0]
	v_pk_mul_f32 v[82:83], v[82:83], v[138:139] op_sel_hi:[1,0]
	s_waitcnt vmcnt(8)
; DI unsigned f2bf(float f) { unsigned u = __builtin_bit_cast(unsigned, f); return (u + 0x7fffu + ((u >> 16) & 1u)) >> 16; }
; template <bool ROUTE, bool COMBINE> ...
;     ...
;     for (int j = 0; j < 4; ++j) {
;         const int c = 8 * lane + 512 * j;
;         const f32x4 oa = v[2 * j] * rstd * *(const f32x4*)(g + c) + *(const f32x4*)(bta + c), ob = v[2 * j + 1] * rstd * *(const f32x4*)(g + c + 4) + *(const f32x4*)(bta + c + 4);
;         if (X) { *(f32x4*)(X + (size_t)row * D_ + c) = oa; *(f32x4*)(X + (size_t)row * D_ + c + 4) = ob; }
;         if (XB) { u32x4 w; w.x = f2bf(oa.x) | (f2bf(oa.y) << 16); w.y = f2bf(oa.z) | (f2bf(oa.w) << 16); w.z = f2bf(ob.x) | (f2bf(ob.y) << 16); w.w = f2bf(ob.z) | (f2bf(ob.w) << 16);
;             *(u32x4*)(XB + (size_t)row * D_ + c) = w; }
;         if (XB8) { const f32x4 sa = oa * 16.f, sb = ob * 16.f;
;             int w0 = __builtin_amdgcn_cvt_pk_fp8_f32(__builtin_amdgcn_fmed3f(sa.x, -448.f, 448.f), __builtin_amdgcn_fmed3f(sa.y, -448.f, 448.f), 0, false);
;             w0 = __builtin_amdgcn_cvt_pk_fp8_f32(__builtin_amdgcn_fmed3f(sa.z, -448.f, 448.f), __builtin_amdgcn_fmed3f(sa.w, -448.f, 448.f), w0, true);
;             int w1 = __builtin_amdgcn_cvt_pk_fp8_f32(__builtin_amdgcn_fmed3f(sb.x, -448.f, 448.f), __builtin_amdgcn_fmed3f(sb.y, -448.f, 448.f), 0, false);
;             w1 = __builtin_amdgcn_cvt_pk_fp8_f32(__builtin_amdgcn_fmed3f(sb.z, -448.f, 448.f), __builtin_amdgcn_fmed3f(sb.w, -448.f, 448.f), w1, true);
;             *(u32x2*)(XB8 + (size_t)row * D_ + c) = (u32x2){(unsigned)w0, (unsigned)w1}; }
	v_pk_fma_f32 v[88:89], v[40:41], v[88:89], v[48:49]
	v_pk_mul_f32 v[90:91], v[106:107], v[138:139] op_sel_hi:[1,0]
	v_bfe_u32 v81, v88, 16, 1
	v_pk_fma_f32 v[106:107], v[38:39], v[82:83], v[46:47]
	v_add3_u32 v81, v88, v81, s17
	v_bfe_u32 v82, v89, 16, 1
	v_pk_fma_f32 v[90:91], v[42:43], v[90:91], v[50:51]
	v_lshrrev_b32_e32 v81, 16, v81
	v_add3_u32 v82, v89, v82, s17
	v_and_or_b32 v82, v82, s3, v81
	v_bfe_u32 v81, v90, 16, 1
	v_pk_mul_f32 v[84:85], v[84:85], v[138:139] op_sel_hi:[1,0]
	v_add3_u32 v81, v90, v81, s17
	v_bfe_u32 v83, v91, 16, 1
	v_pk_fma_f32 v[108:109], v[36:37], v[84:85], v[44:45]
	v_lshrrev_b32_e32 v81, 16, v81
	v_add3_u32 v83, v91, v83, s17
	v_and_or_b32 v83, v83, s3, v81
	v_bfe_u32 v81, v108, 16, 1
	v_bfe_u32 v84, v109, 16, 1
	v_pk_mul_f32 v[88:89], v[88:89], s[16:17] op_sel_hi:[1,0]
	v_add3_u32 v81, v108, v81, s17
	v_add3_u32 v84, v109, v84, s17
	v_pk_mul_f32 v[90:91], v[90:91], s[16:17] op_sel_hi:[1,0]
	v_pk_mul_f32 v[108:109], v[108:109], s[16:17] op_sel_hi:[1,0]
	v_med3_f32 v87, v88, s21, v134
	v_med3_f32 v89, v89, s21, v134
	v_mov_b32_e32 v88, 0
	v_cvt_pk_fp8_f32 v88, v87, v89
	v_med3_f32 v87, v90, s21, v134
	v_med3_f32 v90, v91, s21, v134
	v_med3_f32 v91, v108, s21, v134
	v_med3_f32 v93, v109, s21, v134
	v_mov_b32_e32 v89, 0
	v_cvt_pk_fp8_f32 v89, v91, v93
	v_lshrrev_b32_e32 v81, 16, v81
	v_pk_mul_f32 v[110:111], v[106:107], s[16:17] op_sel_hi:[1,0]
	v_and_or_b32 v84, v84, s3, v81
	v_bfe_u32 v81, v106, 16, 1
	v_cvt_pk_fp8_f32 v88, v87, v90 op_sel:[0,0,1]
	v_med3_f32 v87, v110, s21, v134
	v_med3_f32 v90, v111, s21, v134
	v_add3_u32 v81, v106, v81, s17
	v_bfe_u32 v85, v107, 16, 1
	v_cvt_pk_fp8_f32 v89, v87, v90 op_sel:[0,0,1]
	v_lshrrev_b32_e32 v81, 16, v81
	v_add3_u32 v85, v107, v85, s17
	v_and_or_b32 v85, v85, s3, v81
	global_store_dwordx4 v[142:143], v[82:85], off offset:2048
	global_store_dwordx2 v[118:119], v[88:89], off offset:1024
	v_mov_b32_e32 v81, v92
	v_pk_mul_f32 v[82:83], v[102:103], v[138:139] op_sel_hi:[1,0]
	v_mov_b32_e32 v87, v94
	s_waitcnt vmcnt(6)
	v_pk_fma_f32 v[88:89], v[56:57], v[82:83], v[64:65]
	v_pk_mul_f32 v[80:81], v[80:81], v[138:139] op_sel_hi:[1,0]
	v_pk_mul_f32 v[82:83], v[86:87], v[138:139] op_sel_hi:[1,0]
	v_pk_fma_f32 v[86:87], v[54:55], v[80:81], v[62:63]
	v_bfe_u32 v80, v88, 16, 1
	v_pk_mul_f32 v[84:85], v[104:105], v[138:139] op_sel_hi:[1,0]
	v_add3_u32 v80, v88, v80, s17
	v_bfe_u32 v81, v89, 16, 1
	v_pk_fma_f32 v[84:85], v[58:59], v[84:85], v[66:67]
	v_lshrrev_b32_e32 v80, 16, v80
	v_add3_u32 v81, v89, v81, s17
	v_and_or_b32 v80, v81, s3, v80
	v_bfe_u32 v81, v84, 16, 1
	v_pk_fma_f32 v[90:91], v[52:53], v[82:83], v[60:61]
	v_add3_u32 v81, v84, v81, s17
	v_bfe_u32 v82, v85, 16, 1
	v_lshrrev_b32_e32 v81, 16, v81
	v_add3_u32 v82, v85, v82, s17
	v_and_or_b32 v81, v82, s3, v81
	v_bfe_u32 v82, v90, 16, 1
	v_add3_u32 v82, v90, v82, s17
	v_bfe_u32 v83, v91, 16, 1
	v_lshrrev_b32_e32 v82, 16, v82
	v_add3_u32 v83, v91, v83, s17
	v_and_or_b32 v82, v83, s3, v82
	v_bfe_u32 v83, v86, 16, 1
	v_pk_mul_f32 v[88:89], v[88:89], s[16:17] op_sel_hi:[1,0]
	v_add3_u32 v83, v86, v83, s17
	v_pk_mul_f32 v[92:93], v[86:87], s[16:17] op_sel_hi:[1,0]
	v_pk_mul_f32 v[90:91], v[90:91], s[16:17] op_sel_hi:[1,0]
	v_med3_f32 v86, v88, s21, v134
	v_med3_f32 v89, v89, s21, v134
	v_mov_b32_e32 v88, 0
	v_cvt_pk_fp8_f32 v88, v86, v89
	v_med3_f32 v86, v90, s21, v134
	v_med3_f32 v90, v91, s21, v134
	v_mov_b32_e32 v89, 0
	v_cvt_pk_fp8_f32 v89, v86, v90
	v_pk_mul_f32 v[84:85], v[84:85], s[16:17] op_sel_hi:[1,0]
	v_bfe_u32 v94, v87, 16, 1
	v_med3_f32 v84, v84, s21, v134
	v_med3_f32 v85, v85, s21, v134
	v_cvt_pk_fp8_f32 v88, v84, v85 op_sel:[0,0,1]
	v_med3_f32 v84, v92, s21, v134
	v_med3_f32 v85, v93, s21, v134
	v_cvt_pk_fp8_f32 v89, v84, v85 op_sel:[0,0,1]
	v_lshrrev_b32_e32 v83, 16, v83
	v_add3_u32 v84, v87, v94, s17
	v_and_or_b32 v83, v84, s3, v83
	global_store_dwordx4 v[142:143], v[80:83], off offset:3072
	global_store_dwordx2 v[118:119], v[88:89], off offset:1536
	v_lshl_add_u64 v[96:97], v[96:97], 0, s[12:13]
	s_andn2_b64 vcc, exec, s[18:19]
	v_mov_b32_e32 v92, v76
	v_mov_b32_e32 v93, v77
	v_mov_b32_e32 v94, v78
	v_mov_b32_e32 v95, v79
	v_mov_b32_e32 v80, v72
	v_mov_b32_e32 v81, v73
	v_mov_b32_e32 v82, v74
	v_mov_b32_e32 v83, v75
	v_mov_b32_e32 v84, v68
	v_mov_b32_e32 v85, v69
	v_mov_b32_e32 v86, v70
	v_mov_b32_e32 v87, v71
	v_mov_b32_e32 v88, v0
	v_mov_b32_e32 v89, v1
	v_mov_b32_e32 v90, v2
	v_mov_b32_e32 v91, v3
	s_cbranch_vccz .LBB0_876

; template <bool ROUTE, bool COMBINE> ...
;     ...
;         if (pre) {
; #pragma unroll
;             for (int j = 0; j < 4; ++j) bf8_to_f32(pre[j], v[2 * j], v[2 * j + 1]);
;         } else {
;             const bf16* yr = Yb + (size_t)row * D_ + 8 * lane;
; #pragma unroll
;             for (int j = 0; j < 4; ++j) bf8_to_f32(*(const u32x4*)(yr + 512 * j), v[2 * j], v[2 * j + 1]);
;         }
;     } else {
;         const int p0 = pos[row * 2], p1 = pos[row * 2 + 1]; const float g0 = topg[row * 2], g1 = topg[row * 2 + 1];
; #pragma unroll
;         for (int j = 0; j < 4; ++j) { const int c = 8 * lane + 512 * j;
;             f32x4 xa, xb, pa, pb, a0, a1, c0, c1;
;             bf8_to_f32(*(const u32x4*)(X1B + (size_t)row * D_ + c), xa, xb); bf8_to_f32(*(const u32x4*)(PLEB + (size_t)row * D_ + c), pa, pb);
;             bf8_to_f32(*(const u32x4*)(YE + (size_t)p0 * D_ + c), a0, a1);
;             bf8_to_f32(*(const u32x4*)(YE + (size_t)p1 * D_ + c), c0, c1);
;             v[2 * j] = (ALPHA * xa + (g0 * a0 + g1 * c0)) + pa; v[2 * j + 1] = (ALPHA * xb + (g0 * a1 + g1 * c1)) + pb; }
;     }
; #pragma unroll
;     for (int j = 0; j < 8; ++j) s += (v[j].x + v[j].y) + (v[j].z + v[j].w);
;     const float mean = wave_sum(s) * (1.0f / D_); float s2 = 0.f;
; #pragma unroll
;     for (int j = 0; j < 8; ++j) { v[j] = v[j] - mean; s2 += (v[j].x * v[j].x + v[j].y * v[j].y) + (v[j].z * v[j].z + v[j].w * v[j].w); }
.LBB0_1377:
	s_waitcnt vmcnt(18)
	v_lshlrev_b32_e32 v112, 16, v86
	v_and_b32_e32 v113, 0xffff0000, v86
	v_lshlrev_b32_e32 v114, 16, v87
	v_and_b32_e32 v115, 0xffff0000, v87
	v_lshlrev_b32_e32 v111, 16, v88
	v_lshlrev_b32_e32 v110, 16, v90
	v_and_b32_e32 v127, 0xffff0000, v88
	v_and_b32_e32 v126, 0xffff0000, v90
	v_lshlrev_b32_e32 v87, 16, v89
	v_lshlrev_b32_e32 v86, 16, v91
	v_and_b32_e32 v89, 0xffff0000, v89
	v_and_b32_e32 v88, 0xffff0000, v91
	s_waitcnt vmcnt(17)
	v_lshlrev_b32_e32 v118, 16, v80
	v_and_b32_e32 v122, 0xffff0000, v80
	v_lshlrev_b32_e32 v116, 16, v81
	v_and_b32_e32 v120, 0xffff0000, v81
	v_pk_add_f32 v[80:81], v[110:111], v[126:127]
	v_pk_add_f32 v[90:91], v[86:87], v[88:89]
	v_add_f32_e32 v119, v112, v113
	v_pk_add_f32 v[80:81], v[80:81], v[90:91]
	v_lshlrev_b32_e32 v91, 16, v85
	v_add_f32_e32 v81, 0, v81
	v_add_f32_e32 v121, v80, v81
	v_lshlrev_b32_e32 v90, 16, v84
	v_and_b32_e32 v81, 0xffff0000, v85
	v_and_b32_e32 v80, 0xffff0000, v84
	v_pk_add_f32 v[84:85], v[90:91], v[80:81]
	v_add_f32_e32 v123, v114, v115
	v_pk_add_f32 v[84:85], v[84:85], v[84:85] op_sel_hi:[0,1]
	v_mov_b32_e32 v117, v85
	v_pk_add_f32 v[124:125], v[118:119], v[122:123]
	v_pk_add_f32 v[84:85], v[116:117], v[120:121]
	s_waitcnt vmcnt(16)
	v_lshlrev_b32_e32 v106, 16, v92
	v_pk_add_f32 v[84:85], v[124:125], v[84:85]
	v_lshlrev_b32_e32 v125, 16, v83
	v_lshlrev_b32_e32 v124, 16, v82
	v_and_b32_e32 v83, 0xffff0000, v83
	v_and_b32_e32 v82, 0xffff0000, v82
	v_pk_add_f32 v[138:139], v[124:125], v[82:83]
	v_and_b32_e32 v107, 0xffff0000, v92
	v_lshlrev_b32_e32 v108, 16, v93
	v_and_b32_e32 v109, 0xffff0000, v93
	v_pk_add_f32 v[84:85], v[84:85], v[84:85] op_sel_hi:[0,1]
	v_pk_add_f32 v[138:139], v[138:139], v[138:139] op_sel_hi:[0,1]
	v_lshlrev_b32_e32 v102, 16, v94
	v_and_b32_e32 v104, 0xffff0000, v94
	v_lshlrev_b32_e32 v92, 16, v95
	v_and_b32_e32 v94, 0xffff0000, v95
	v_add_f32_e32 v103, v106, v107
	v_add_f32_e32 v105, v108, v109
	v_mov_b32_e32 v93, v139
	v_mov_b32_e32 v95, v85
	v_pk_add_f32 v[140:141], v[102:103], v[104:105]
	v_pk_add_f32 v[84:85], v[92:93], v[94:95]
	s_ashr_i32 s17, s16, 31
	v_pk_add_f32 v[84:85], v[140:141], v[84:85]
	s_lshl_b64 s[8:9], s[16:17], 12
	v_add_f32_e32 v84, v84, v85
	v_mov_b32_e32 v93, v84
	s_nop 1
	v_add_f32_dpp v93, v93, v93 quad_perm:[1,0,3,2] row_mask:0xf bank_mask:0xf
	s_nop 1
	v_add_f32_dpp v93, v93, v93 quad_perm:[2,3,0,1] row_mask:0xf bank_mask:0xf
	s_nop 1
	v_add_f32_dpp v93, v93, v93 row_half_mirror row_mask:0xf bank_mask:0xf
	s_nop 1
	v_add_f32_dpp v93, v93, v93 row_mirror row_mask:0xf bank_mask:0xf
	s_nop 1
	v_add_f32_dpp v93, v93, v93 row_bcast:15 row_mask:0xa bank_mask:0xf
	s_nop 1
	v_add_f32_dpp v93, v93, v93 row_bcast:31 row_mask:0xc bank_mask:0xf
	s_nop 1
	v_readlane_b32 s98, v93, 63
	s_nop 3
	v_mov_b32_e32 v93, s98
	v_lshl_add_u64 v[148:149], v[100:101], 0, s[8:9]
	s_waitcnt lgkmcnt(0)
	v_fmac_f32_e32 v127, 0xba000000, v93
	v_fmac_f32_e32 v126, 0xba000000, v93
	v_fmac_f32_e32 v89, 0xba000000, v93
	v_fmac_f32_e32 v111, 0xba000000, v93
	v_fmac_f32_e32 v88, 0xba000000, v93
	v_fmac_f32_e32 v110, 0xba000000, v93
	v_mov_b32_e32 v138, v127
	v_mov_b32_e32 v139, v126
	v_fmac_f32_e32 v87, 0xba000000, v93
	v_fmac_f32_e32 v86, 0xba000000, v93
	v_mov_b32_e32 v84, v111
	v_mov_b32_e32 v85, v110
	v_pk_mul_f32 v[138:139], v[138:139], v[138:139]
	v_mov_b32_e32 v140, v89
	v_mov_b32_e32 v141, v88
	v_pk_fma_f32 v[84:85], v[84:85], v[84:85], v[138:139]
	v_mov_b32_e32 v138, v87
	v_mov_b32_e32 v139, v86
	v_pk_mul_f32 v[140:141], v[140:141], v[140:141]
	v_fmac_f32_e32 v80, 0xba000000, v93
	v_fmac_f32_e32 v81, 0xba000000, v93
	v_fmac_f32_e32 v91, 0xba000000, v93
	v_pk_fma_f32 v[138:139], v[138:139], v[138:139], v[140:141]
	v_fmac_f32_e32 v90, 0xba000000, v93
	v_mov_b32_e32 v142, v91
	v_mov_b32_e32 v143, v81
	v_mov_b32_e32 v91, v80
	v_pk_add_f32 v[84:85], v[84:85], v[138:139]
	v_pk_mul_f32 v[138:139], v[142:143], v[142:143]
	v_pk_mul_f32 v[80:81], v[90:91], v[90:91]
	v_fmac_f32_e32 v112, 0xba000000, v93
	v_pk_mov_b32 v[140:141], v[80:81], v[138:139] op_sel:[1,0]
	v_mov_b32_e32 v81, v139
	v_pk_add_f32 v[80:81], v[140:141], v[80:81]
	v_fmac_f32_e32 v113, 0xba000000, v93
	v_pk_add_f32 v[80:81], v[80:81], v[80:81] op_sel_hi:[0,1]
	v_fmac_f32_e32 v114, 0xba000000, v93
	v_mul_f32_e32 v80, v112, v112
	v_fmac_f32_e32 v115, 0xba000000, v93
	v_pk_fma_f32 v[138:139], v[112:113], v[112:113], v[80:81] op_sel_hi:[1,1,0]
	v_mul_f32_e32 v80, v114, v114
	v_pk_add_f32 v[84:85], v[84:85], v[84:85] op_sel_hi:[0,1]
	v_pk_fma_f32 v[140:141], v[114:115], v[114:115], v[80:81] op_sel_hi:[1,1,0]
	v_fmac_f32_e32 v120, 0xba000000, v93
	v_fmac_f32_e32 v116, 0xba000000, v93
	v_fmac_f32_e32 v122, 0xba000000, v93
	v_fmac_f32_e32 v118, 0xba000000, v93
	v_mul_f32_e32 v138, v118, v118
	v_mul_f32_e32 v140, v122, v122
	v_mul_f32_e32 v80, v116, v116
	v_mul_f32_e32 v84, v120, v120
	v_pk_add_f32 v[138:139], v[138:139], v[140:141]
	v_pk_add_f32 v[80:81], v[80:81], v[84:85]
	v_fmac_f32_e32 v82, 0xba000000, v93
	v_fmac_f32_e32 v83, 0xba000000, v93
	v_fmac_f32_e32 v125, 0xba000000, v93
	v_pk_add_f32 v[80:81], v[138:139], v[80:81]
	v_fmac_f32_e32 v124, 0xba000000, v93
	v_mov_b32_e32 v144, v125
	v_mov_b32_e32 v145, v83
	v_mov_b32_e32 v125, v82
	v_pk_add_f32 v[80:81], v[80:81], v[80:81] op_sel_hi:[0,1]
	v_pk_mul_f32 v[84:85], v[144:145], v[144:145]
	v_pk_mul_f32 v[82:83], v[124:125], v[124:125]
	v_fmac_f32_e32 v106, 0xba000000, v93
	v_pk_mov_b32 v[138:139], v[82:83], v[84:85] op_sel:[1,0]
	v_mov_b32_e32 v83, v85
	v_fmac_f32_e32 v107, 0xba000000, v93
	v_fmac_f32_e32 v108, 0xba000000, v93
	v_mul_f32_e32 v80, v106, v106
	v_pk_add_f32 v[82:83], v[138:139], v[82:83]
	v_fmac_f32_e32 v109, 0xba000000, v93
; DI unsigned f2bf(float f) { unsigned u = __builtin_bit_cast(unsigned, f); return (u + 0x7fffu + ((u >> 16) & 1u)) >> 16; }
; template <bool ROUTE, bool COMBINE> ...
;     ...
;     for (int j = 0; j < 8; ++j) { v[j] = v[j] - mean; s2 += (v[j].x * v[j].x + v[j].y * v[j].y) + (v[j].z * v[j].z + v[j].w * v[j].w); }
;     const float rstd = 1.0f / sqrtf(wave_sum(s2) * (1.0f / D_) + LN_EPS);
;     float lg0 = 0.f, lg1 = 0.f, lg2 = 0.f, lg3 = 0.f, lg4 = 0.f, lg5 = 0.f, lg6 = 0.f, lg7 = 0.f;
; #pragma unroll
;     for (int j = 0; j < 4; ++j) {
;         const int c = 8 * lane + 512 * j;
;         const f32x4 oa = v[2 * j] * rstd * *(const f32x4*)(g + c) + *(const f32x4*)(bta + c), ob = v[2 * j + 1] * rstd * *(const f32x4*)(g + c + 4) + *(const f32x4*)(bta + c + 4);
;         if (X) { *(f32x4*)(X + (size_t)row * D_ + c) = oa; *(f32x4*)(X + (size_t)row * D_ + c + 4) = ob; }
;         if (XB) { u32x4 w; w.x = f2bf(oa.x) | (f2bf(oa.y) << 16); w.y = f2bf(oa.z) | (f2bf(oa.w) << 16); w.z = f2bf(ob.x) | (f2bf(ob.y) << 16); w.w = f2bf(ob.z) | (f2bf(ob.w) << 16);
;             *(u32x4*)(XB + (size_t)row * D_ + c) = w; }
	v_pk_fma_f32 v[84:85], v[106:107], v[106:107], v[80:81] op_sel_hi:[1,1,0]
	v_mul_f32_e32 v80, v108, v108
	v_pk_add_f32 v[82:83], v[82:83], v[82:83] op_sel_hi:[0,1]
	v_pk_fma_f32 v[138:139], v[108:109], v[108:109], v[80:81] op_sel_hi:[1,1,0]
	v_fmac_f32_e32 v94, 0xba000000, v93
	v_fmac_f32_e32 v92, 0xba000000, v93
	v_fmac_f32_e32 v104, 0xba000000, v93
	v_fmac_f32_e32 v102, 0xba000000, v93
	v_mul_f32_e32 v84, v102, v102
	v_mul_f32_e32 v138, v104, v104
	v_mul_f32_e32 v82, v92, v92
	v_mul_f32_e32 v80, v94, v94
	v_pk_add_f32 v[84:85], v[84:85], v[138:139]
	v_pk_add_f32 v[80:81], v[82:83], v[80:81]
	v_mov_b32_e32 v138, v110
	v_pk_add_f32 v[80:81], v[84:85], v[80:81]
	v_mov_b32_e32 v110, v86
	v_add_f32_e32 v80, v80, v81
	v_mov_b32_e32 v81, v80
	s_nop 1
	v_add_f32_dpp v81, v81, v81 quad_perm:[1,0,3,2] row_mask:0xf bank_mask:0xf
	s_nop 1
	v_add_f32_dpp v81, v81, v81 quad_perm:[2,3,0,1] row_mask:0xf bank_mask:0xf
	s_nop 1
	v_add_f32_dpp v81, v81, v81 row_half_mirror row_mask:0xf bank_mask:0xf
	s_nop 1
	v_add_f32_dpp v81, v81, v81 row_mirror row_mask:0xf bank_mask:0xf
	s_nop 1
	v_add_f32_dpp v81, v81, v81 row_bcast:15 row_mask:0xa bank_mask:0xf
	s_nop 1
	v_add_f32_dpp v81, v81, v81 row_bcast:31 row_mask:0xc bank_mask:0xf
	s_nop 1
	v_readlane_b32 s98, v81, 63
	s_nop 3
	v_mov_b32_e32 v81, s98
	v_mov_b32_e32 v139, v126
	v_mov_b32_e32 v126, v111
	v_mov_b32_e32 v111, v88
	v_mov_b32_e32 v88, v87
	s_waitcnt lgkmcnt(0)
	v_mov_b32_e32 v119, v122
	v_mov_b32_e32 v117, v120
	v_mov_b32_e32 v103, v104
	v_mov_b32_e32 v80, 0
	v_fmamk_f32 v81, v81, 0x3a000000, v96
	v_mul_f32_e32 v82, 0x4f800000, v81
	v_cmp_gt_f32_e32 vcc, s28, v81
	s_nop 1
	v_cndmask_b32_e32 v81, v81, v82, vcc
	v_sqrt_f32_e32 v82, v81
	s_nop 0
	v_add_u32_e32 v83, -1, v82
	v_fma_f32 v84, -v83, v82, v81
	v_cmp_ge_f32_e64 s[6:7], 0, v84
	v_add_u32_e32 v84, 1, v82
	s_nop 0
	v_cndmask_b32_e64 v83, v82, v83, s[6:7]
	v_fma_f32 v82, -v84, v82, v81
	v_cmp_lt_f32_e64 s[6:7], 0, v82
	s_nop 1
	v_cndmask_b32_e64 v82, v83, v84, s[6:7]
	v_mul_f32_e32 v83, 0x37800000, v82
	v_cndmask_b32_e32 v82, v82, v83, vcc
	v_cmp_class_f32_e32 vcc, v81, v135
	s_nop 1
	v_cndmask_b32_e32 v81, v82, v81, vcc
	v_div_scale_f32 v82, s[6:7], v81, v81, 1.0
	v_rcp_f32_e32 v83, v82
	s_mov_b32 s6, 0
	s_mov_b32 s7, 0
	v_fma_f32 v84, -v82, v83, 1.0
	v_fmac_f32_e32 v83, v84, v83
	v_div_scale_f32 v84, vcc, 1.0, v81, 1.0
	v_mul_f32_e32 v85, v84, v83
	v_fma_f32 v86, -v82, v85, v84
	v_fmac_f32_e32 v85, v86, v83
	v_fma_f32 v82, -v82, v85, v84
	v_div_fmas_f32 v82, v82, v83, v85
	v_div_fixup_f32 v146, v82, v81, 1.0
	v_pk_mul_f32 v[84:85], v[126:127], v[146:147] op_sel_hi:[1,0]
	v_pk_mul_f32 v[82:83], v[88:89], v[146:147] op_sel_hi:[1,0]
	s_waitcnt vmcnt(12)
	v_pk_fma_f32 v[84:85], v[4:5], v[84:85], v[12:13]
	v_pk_fma_f32 v[82:83], v[6:7], v[82:83], v[14:15]
	v_bfe_u32 v81, v84, 16, 1
	v_add3_u32 v81, v84, v81, s29
	v_bfe_u32 v93, v85, 16, 1
	v_lshrrev_b32_e32 v81, 16, v81
	v_add3_u32 v93, v85, v93, s29
	v_pk_mul_f32 v[88:89], v[138:139], v[146:147] op_sel_hi:[1,0]
	v_and_or_b32 v138, v93, s27, v81
	v_bfe_u32 v81, v82, 16, 1
	v_add3_u32 v81, v82, v81, s29
	v_bfe_u32 v93, v83, 16, 1
	v_pk_fma_f32 v[88:89], v[0:1], v[88:89], v[8:9]
	v_lshrrev_b32_e32 v81, 16, v81
	v_add3_u32 v93, v83, v93, s29
	v_and_or_b32 v139, v93, s27, v81
	v_bfe_u32 v81, v88, 16, 1
	v_pk_mul_f32 v[86:87], v[110:111], v[146:147] op_sel_hi:[1,0]
	v_add3_u32 v81, v88, v81, s29
	v_bfe_u32 v93, v89, 16, 1
	v_pk_fma_f32 v[86:87], v[2:3], v[86:87], v[10:11]
	v_lshrrev_b32_e32 v81, 16, v81
	v_add3_u32 v93, v89, v93, s29
	v_and_or_b32 v140, v93, s27, v81
	v_bfe_u32 v81, v86, 16, 1
	v_add3_u32 v81, v86, v81, s29
	v_bfe_u32 v93, v87, 16, 1
	v_pk_mul_f32 v[110:111], v[90:91], v[146:147] op_sel_hi:[1,0]
	v_lshrrev_b32_e32 v81, 16, v81
	v_add3_u32 v93, v87, v93, s29
	s_waitcnt vmcnt(8)
; DI unsigned f2bf(float f) { unsigned u = __builtin_bit_cast(unsigned, f); return (u + 0x7fffu + ((u >> 16) & 1u)) >> 16; }
; template <bool ROUTE, bool COMBINE> ...
;     ...
;     for (int j = 0; j < 4; ++j) {
;         const int c = 8 * lane + 512 * j;
;         const f32x4 oa = v[2 * j] * rstd * *(const f32x4*)(g + c) + *(const f32x4*)(bta + c), ob = v[2 * j + 1] * rstd * *(const f32x4*)(g + c + 4) + *(const f32x4*)(bta + c + 4);
;         if (X) { *(f32x4*)(X + (size_t)row * D_ + c) = oa; *(f32x4*)(X + (size_t)row * D_ + c + 4) = ob; }
;         if (XB) { u32x4 w; w.x = f2bf(oa.x) | (f2bf(oa.y) << 16); w.y = f2bf(oa.z) | (f2bf(oa.w) << 16); w.z = f2bf(ob.x) | (f2bf(ob.y) << 16); w.w = f2bf(ob.z) | (f2bf(ob.w) << 16);
;             *(u32x4*)(XB + (size_t)row * D_ + c) = w; }
;         if (XB8) { const f32x4 sa = oa * 16.f, sb = ob * 16.f;
;             int w0 = __builtin_amdgcn_cvt_pk_fp8_f32(__builtin_amdgcn_fmed3f(sa.x, -448.f, 448.f), __builtin_amdgcn_fmed3f(sa.y, -448.f, 448.f), 0, false);
;             w0 = __builtin_amdgcn_cvt_pk_fp8_f32(__builtin_amdgcn_fmed3f(sa.z, -448.f, 448.f), __builtin_amdgcn_fmed3f(sa.w, -448.f, 448.f), w0, true);
;             int w1 = __builtin_amdgcn_cvt_pk_fp8_f32(__builtin_amdgcn_fmed3f(sb.x, -448.f, 448.f), __builtin_amdgcn_fmed3f(sb.y, -448.f, 448.f), 0, false);
;             w1 = __builtin_amdgcn_cvt_pk_fp8_f32(__builtin_amdgcn_fmed3f(sb.z, -448.f, 448.f), __builtin_amdgcn_fmed3f(sb.w, -448.f, 448.f), w1, true);
;             *(u32x2*)(XB8 + (size_t)row * D_ + c) = (u32x2){(unsigned)w0, (unsigned)w1}; }
;         if (ROUTE) { v[2 * j] = oa; v[2 * j + 1] = ob; }
	v_pk_fma_f32 v[110:111], v[20:21], v[110:111], v[28:29]
	v_and_or_b32 v141, v93, s27, v81
	v_bfe_u32 v81, v110, 16, 1
	v_pk_mul_f32 v[90:91], v[142:143], v[146:147] op_sel_hi:[1,0]
	v_add3_u32 v81, v110, v81, s29
	v_bfe_u32 v93, v111, 16, 1
	v_pk_fma_f32 v[90:91], v[22:23], v[90:91], v[30:31]
	v_lshrrev_b32_e32 v81, 16, v81
	v_add3_u32 v93, v111, v93, s29
	global_store_dwordx4 v[148:149], v[138:141], off
	v_pk_mul_f32 v[126:127], v[112:113], v[146:147] op_sel_hi:[1,0]
	v_pk_mul_f32 v[112:113], v[114:115], v[146:147] op_sel_hi:[1,0]
	v_and_or_b32 v138, v93, s27, v81
	v_bfe_u32 v81, v90, 16, 1
	v_add3_u32 v81, v90, v81, s29
	v_bfe_u32 v93, v91, 16, 1
	v_pk_fma_f32 v[114:115], v[16:17], v[126:127], v[24:25]
	v_lshrrev_b32_e32 v81, 16, v81
	v_add3_u32 v93, v91, v93, s29
	v_and_or_b32 v139, v93, s27, v81
	v_bfe_u32 v81, v114, 16, 1
	v_add3_u32 v81, v114, v81, s29
	v_bfe_u32 v93, v115, 16, 1
	v_pk_fma_f32 v[112:113], v[18:19], v[112:113], v[26:27]
	v_lshrrev_b32_e32 v81, 16, v81
	v_add3_u32 v93, v115, v93, s29
	v_and_or_b32 v140, v93, s27, v81
	v_bfe_u32 v81, v112, 16, 1
	v_add3_u32 v81, v112, v81, s29
	v_bfe_u32 v93, v113, 16, 1
	v_pk_mul_f32 v[118:119], v[118:119], v[146:147] op_sel_hi:[1,0]
	v_lshrrev_b32_e32 v81, 16, v81
	v_add3_u32 v93, v113, v93, s29
	s_waitcnt vmcnt(5)
	v_pk_fma_f32 v[118:119], v[36:37], v[118:119], v[44:45]
	v_and_or_b32 v141, v93, s27, v81
	v_bfe_u32 v81, v118, 16, 1
	v_pk_mul_f32 v[116:117], v[116:117], v[146:147] op_sel_hi:[1,0]
	v_add3_u32 v81, v118, v81, s29
	v_bfe_u32 v93, v119, 16, 1
	v_pk_fma_f32 v[116:117], v[38:39], v[116:117], v[46:47]
	v_lshrrev_b32_e32 v81, 16, v81
	v_add3_u32 v93, v119, v93, s29
	v_pk_mul_f32 v[122:123], v[124:125], v[146:147] op_sel_hi:[1,0]
	v_and_or_b32 v124, v93, s27, v81
	v_bfe_u32 v81, v116, 16, 1
	v_add3_u32 v81, v116, v81, s29
	v_bfe_u32 v93, v117, 16, 1
	v_pk_fma_f32 v[122:123], v[32:33], v[122:123], v[40:41]
	v_lshrrev_b32_e32 v81, 16, v81
	v_add3_u32 v93, v117, v93, s29
	v_and_or_b32 v125, v93, s27, v81
	v_bfe_u32 v81, v122, 16, 1
	v_pk_mul_f32 v[120:121], v[144:145], v[146:147] op_sel_hi:[1,0]
	v_add3_u32 v81, v122, v81, s29
	v_bfe_u32 v93, v123, 16, 1
	v_pk_fma_f32 v[120:121], v[34:35], v[120:121], v[42:43]
	v_lshrrev_b32_e32 v81, 16, v81
	v_add3_u32 v93, v123, v93, s29
	v_and_or_b32 v126, v93, s27, v81
	v_bfe_u32 v81, v120, 16, 1
	v_add3_u32 v81, v120, v81, s29
	v_bfe_u32 v93, v121, 16, 1
	v_lshrrev_b32_e32 v81, 16, v81
	v_add3_u32 v93, v121, v93, s29
	v_and_or_b32 v127, v93, s27, v81
	global_store_dwordx4 v[148:149], v[124:127], off offset:2048
	v_mov_b32_e32 v93, v94
	v_pk_mul_f32 v[92:93], v[92:93], v[146:147] op_sel_hi:[1,0]
	v_pk_mul_f32 v[124:125], v[106:107], v[146:147] op_sel_hi:[1,0]
	v_pk_mul_f32 v[106:107], v[108:109], v[146:147] op_sel_hi:[1,0]
	s_waitcnt vmcnt(2)
	v_pk_fma_f32 v[108:109], v[52:53], v[124:125], v[60:61]
	v_pk_mul_f32 v[104:105], v[102:103], v[146:147] op_sel_hi:[1,0]
	v_bfe_u32 v81, v108, 16, 1
	v_pk_fma_f32 v[102:103], v[50:51], v[92:93], v[58:59]
	v_add3_u32 v81, v108, v81, s29
	v_bfe_u32 v92, v109, 16, 1
	v_pk_fma_f32 v[106:107], v[54:55], v[106:107], v[62:63]
	v_lshrrev_b32_e32 v81, 16, v81
	v_add3_u32 v92, v109, v92, s29
	v_and_or_b32 v92, v92, s27, v81
	v_bfe_u32 v81, v106, 16, 1
	v_add3_u32 v81, v106, v81, s29
	v_bfe_u32 v93, v107, 16, 1
	v_pk_fma_f32 v[104:105], v[48:49], v[104:105], v[56:57]
	v_lshrrev_b32_e32 v81, 16, v81
	v_add3_u32 v93, v107, v93, s29
	v_and_or_b32 v93, v93, s27, v81
	v_bfe_u32 v81, v104, 16, 1
	v_add3_u32 v81, v104, v81, s29
	v_bfe_u32 v94, v105, 16, 1
	v_lshrrev_b32_e32 v81, 16, v81
	v_add3_u32 v94, v105, v94, s29
	v_and_or_b32 v94, v94, s27, v81
	v_bfe_u32 v81, v102, 16, 1
	v_add3_u32 v81, v102, v81, s29
	v_bfe_u32 v95, v103, 16, 1
	v_lshrrev_b32_e32 v81, 16, v81
	v_add3_u32 v95, v103, v95, s29
	v_and_or_b32 v95, v95, s27, v81
	global_store_dwordx4 v[148:149], v[92:95], off offset:3072
	v_mov_b32_e32 v81, v80
	v_mov_b32_e32 v124, v80
	v_mov_b32_e32 v125, v80
	v_mov_b32_e32 v94, v80
	v_mov_b32_e32 v95, v80
	v_mov_b32_e32 v92, v80
	v_mov_b32_e32 v93, v80
	global_store_dwordx4 v[148:149], v[138:141], off offset:1024

; template <bool ROUTE, bool COMBINE> ...
;     ...
;         const int p0 = pos[row * 2], p1 = pos[row * 2 + 1]; const float g0 = topg[row * 2], g1 = topg[row * 2 + 1];
; #pragma unroll
;         for (int j = 0; j < 4; ++j) { const int c = 8 * lane + 512 * j;
;             f32x4 xa, xb, pa, pb, a0, a1, c0, c1;
;             bf8_to_f32(*(const u32x4*)(X1B + (size_t)row * D_ + c), xa, xb); bf8_to_f32(*(const u32x4*)(PLEB + (size_t)row * D_ + c), pa, pb);
;             bf8_to_f32(*(const u32x4*)(YE + (size_t)p0 * D_ + c), a0, a1);
;             bf8_to_f32(*(const u32x4*)(YE + (size_t)p1 * D_ + c), c0, c1);
;             v[2 * j] = (ALPHA * xa + (g0 * a0 + g1 * c0)) + pa; v[2 * j + 1] = (ALPHA * xb + (g0 * a1 + g1 * c1)) + pb; }
.LBB0_1775:
	s_ashr_i32 s11, s10, 31
	s_lshl_b64 s[2:3], s[10:11], 2
	s_add_u32 s16, s19, s2
	s_addc_u32 s17, s20, s3
	global_load_dwordx2 v[54:55], v5, s[16:17]
	global_load_dwordx4 v[0:3], v[26:27], off offset:-3072
	global_load_dwordx4 v[28:31], v[26:27], off offset:-2048
	global_load_dwordx4 v[32:35], v[26:27], off offset:-1024
	s_add_i32 s16, s10, 1
	s_ashr_i32 s17, s16, 31
	s_add_u32 s2, s15, s2
	s_waitcnt vmcnt(15)
	v_add_co_u32_e32 v84, vcc, s7, v26
	s_addc_u32 s3, s18, s3
	s_lshl_b64 s[16:17], s[16:17], 2
	v_addc_co_u32_e32 v85, vcc, -1, v27, vcc
	s_add_u32 s16, s15, s16
	global_load_dwordx4 v[36:39], v[84:85], off offset:-3072
	global_load_dwordx4 v[40:43], v[84:85], off offset:-2048
	global_load_dwordx4 v[46:49], v[84:85], off offset:-1024
	s_addc_u32 s17, s18, s17
	global_load_dword v4, v5, s[2:3]
	global_load_dword v44, v5, s[16:17]
	s_and_b64 vcc, exec, s[0:1]
	s_waitcnt vmcnt(8)
	v_ashrrev_i32_e32 v51, 31, v54
	v_mov_b32_e32 v50, v54
	v_ashrrev_i32_e32 v65, 31, v55
	s_waitcnt lgkmcnt(0)
	v_mov_b32_e32 v64, v55
	v_lshlrev_b64 v[50:51], 12, v[50:51]
	v_lshlrev_b64 v[54:55], 12, v[64:65]
	v_lshl_add_u64 v[92:93], v[22:23], 0, v[50:51]
	v_lshl_add_u64 v[54:55], v[22:23], 0, v[54:55]
	global_load_dwordx4 v[50:53], v[92:93], off
	global_load_dwordx4 v[64:67], v[54:55], off
	global_load_dwordx4 v[68:71], v[92:93], off offset:1024
	global_load_dwordx4 v[72:75], v[54:55], off offset:1024
	global_load_dwordx4 v[76:79], v[26:27], off
	global_load_dwordx4 v[80:83], v[84:85], off
	s_waitcnt vmcnt(13)
	v_lshlrev_b32_e32 v94, 16, v0
	v_and_b32_e32 v95, 0xffff0000, v0
	v_lshlrev_b32_e32 v96, 16, v1
	v_and_b32_e32 v97, 0xffff0000, v1
	global_load_dwordx4 v[84:87], v[92:93], off offset:2048
	v_lshlrev_b32_e32 v98, 16, v2
	v_and_b32_e32 v99, 0xffff0000, v2
	v_lshlrev_b32_e32 v100, 16, v3
	v_and_b32_e32 v101, 0xffff0000, v3
	global_load_dwordx4 v[0:3], v[54:55], off offset:2048
	s_waitcnt vmcnt(13)
	v_lshlrev_b32_e32 v106, 16, v32
	v_and_b32_e32 v107, 0xffff0000, v32
	v_lshlrev_b32_e32 v108, 16, v33
	v_and_b32_e32 v109, 0xffff0000, v33
	v_lshlrev_b32_e32 v110, 16, v34
	v_and_b32_e32 v111, 0xffff0000, v34
	v_lshlrev_b32_e32 v112, 16, v35
	v_and_b32_e32 v113, 0xffff0000, v35
	global_load_dwordx4 v[32:35], v[92:93], off offset:3072
	global_load_dwordx4 v[88:91], v[54:55], off offset:3072
	s_waitcnt vmcnt(12)
	v_lshlrev_b32_e32 v124, 16, v48
	v_and_b32_e32 v125, 0xffff0000, v48
	v_lshlrev_b32_e32 v126, 16, v49
	v_and_b32_e32 v127, 0xffff0000, v49
	v_lshlrev_b32_e32 v114, 16, v36
	v_and_b32_e32 v115, 0xffff0000, v36
	v_lshlrev_b32_e32 v36, 16, v37
	v_and_b32_e32 v37, 0xffff0000, v37
	v_lshlrev_b32_e32 v118, 16, v40
	v_and_b32_e32 v119, 0xffff0000, v40
	v_lshlrev_b32_e32 v40, 16, v41
	v_and_b32_e32 v41, 0xffff0000, v41
	v_lshlrev_b32_e32 v102, 16, v28
	v_and_b32_e32 v103, 0xffff0000, v28
	v_lshlrev_b32_e32 v28, 16, v29
	v_and_b32_e32 v29, 0xffff0000, v29
	v_lshlrev_b32_e32 v116, 16, v38
	v_and_b32_e32 v117, 0xffff0000, v38
	v_lshlrev_b32_e32 v38, 16, v39
	v_and_b32_e32 v39, 0xffff0000, v39
	v_lshlrev_b32_e32 v120, 16, v42
	v_and_b32_e32 v121, 0xffff0000, v42
	v_lshlrev_b32_e32 v42, 16, v43
	v_and_b32_e32 v43, 0xffff0000, v43
	v_lshlrev_b32_e32 v104, 16, v30
	v_and_b32_e32 v105, 0xffff0000, v30
	v_lshlrev_b32_e32 v30, 16, v31
	v_and_b32_e32 v31, 0xffff0000, v31
	v_lshlrev_b32_e32 v122, 16, v46
	v_and_b32_e32 v123, 0xffff0000, v46
	v_lshlrev_b32_e32 v46, 16, v47
	v_and_b32_e32 v47, 0xffff0000, v47
	s_waitcnt vmcnt(8)
	v_lshlrev_b32_e32 v92, 16, v64
	v_and_b32_e32 v93, 0xffff0000, v64
	v_lshlrev_b32_e32 v64, 16, v65
	v_and_b32_e32 v65, 0xffff0000, v65
	v_lshlrev_b32_e32 v128, 16, v66
	v_and_b32_e32 v129, 0xffff0000, v66
	v_lshlrev_b32_e32 v66, 16, v67
	v_and_b32_e32 v67, 0xffff0000, v67
	s_waitcnt vmcnt(6)
	v_lshlrev_b32_e32 v134, 16, v72
	v_and_b32_e32 v135, 0xffff0000, v72
	v_lshlrev_b32_e32 v72, 16, v73
	v_and_b32_e32 v73, 0xffff0000, v73
	v_lshlrev_b32_e32 v48, 16, v50
	v_and_b32_e32 v49, 0xffff0000, v50
	v_lshlrev_b32_e32 v50, 16, v51
	v_and_b32_e32 v51, 0xffff0000, v51
	v_lshlrev_b32_e32 v54, 16, v52
	v_and_b32_e32 v55, 0xffff0000, v52
	v_lshlrev_b32_e32 v52, 16, v53
	v_and_b32_e32 v53, 0xffff0000, v53
	v_lshlrev_b32_e32 v130, 16, v68
	v_and_b32_e32 v131, 0xffff0000, v68
	v_lshlrev_b32_e32 v68, 16, v69
	v_and_b32_e32 v69, 0xffff0000, v69
	v_lshlrev_b32_e32 v136, 16, v74
	v_and_b32_e32 v137, 0xffff0000, v74
	v_lshlrev_b32_e32 v74, 16, v75
	v_and_b32_e32 v75, 0xffff0000, v75
	s_waitcnt vmcnt(2)
; template <bool ROUTE, bool COMBINE> ...
;     ...
;         const int p0 = pos[row * 2], p1 = pos[row * 2 + 1]; const float g0 = topg[row * 2], g1 = topg[row * 2 + 1];
; #pragma unroll
;         for (int j = 0; j < 4; ++j) { const int c = 8 * lane + 512 * j;
;             f32x4 xa, xb, pa, pb, a0, a1, c0, c1;
;             bf8_to_f32(*(const u32x4*)(X1B + (size_t)row * D_ + c), xa, xb); bf8_to_f32(*(const u32x4*)(PLEB + (size_t)row * D_ + c), pa, pb);
;             bf8_to_f32(*(const u32x4*)(YE + (size_t)p0 * D_ + c), a0, a1);
;             bf8_to_f32(*(const u32x4*)(YE + (size_t)p1 * D_ + c), c0, c1);
;             v[2 * j] = (ALPHA * xa + (g0 * a0 + g1 * c0)) + pa; v[2 * j + 1] = (ALPHA * xb + (g0 * a1 + g1 * c1)) + pb; }
	v_lshlrev_b32_e32 v144, 16, v2
	v_and_b32_e32 v145, 0xffff0000, v2
	v_lshlrev_b32_e32 v146, 16, v3
	v_and_b32_e32 v147, 0xffff0000, v3
	v_pk_mul_f32 v[2:3], v[44:45], v[92:93] op_sel_hi:[0,1]
	v_pk_mul_f32 v[64:65], v[44:45], v[64:65] op_sel_hi:[0,1]
	v_pk_mul_f32 v[92:93], v[44:45], v[128:129] op_sel_hi:[0,1]
	v_pk_mul_f32 v[66:67], v[44:45], v[66:67] op_sel_hi:[0,1]
	v_pk_mul_f32 v[72:73], v[44:45], v[72:73] op_sel_hi:[0,1]
	v_lshlrev_b32_e32 v132, 16, v70
	v_and_b32_e32 v133, 0xffff0000, v70
	v_lshlrev_b32_e32 v70, 16, v71
	v_and_b32_e32 v71, 0xffff0000, v71
	v_pk_mul_f32 v[74:75], v[44:45], v[74:75] op_sel_hi:[0,1]
	v_pk_fma_f32 v[50:51], v[4:5], v[50:51], v[64:65] op_sel_hi:[0,1,1]
	v_pk_fma_f32 v[2:3], v[4:5], v[48:49], v[2:3] op_sel_hi:[0,1,1]
	v_pk_fma_f32 v[48:49], v[4:5], v[52:53], v[66:67] op_sel_hi:[0,1,1]
	v_pk_fma_f32 v[52:53], v[4:5], v[54:55], v[92:93] op_sel_hi:[0,1,1]
	v_pk_fma_f32 v[54:55], v[4:5], v[68:69], v[72:73] op_sel_hi:[0,1,1]
	v_lshlrev_b32_e32 v142, 16, v0
	v_and_b32_e32 v143, 0xffff0000, v0
	v_lshlrev_b32_e32 v0, 16, v1
	v_and_b32_e32 v1, 0xffff0000, v1
	v_pk_fma_f32 v[66:67], v[4:5], v[70:71], v[74:75] op_sel_hi:[0,1,1]
	v_pk_fma_f32 v[36:37], v[36:37], s[14:15], v[50:51] op_sel_hi:[1,0,1]
	v_pk_fma_f32 v[40:41], v[40:41], s[14:15], v[54:55] op_sel_hi:[1,0,1]
	v_lshlrev_b32_e32 v138, 16, v84
	v_and_b32_e32 v139, 0xffff0000, v84
	v_lshlrev_b32_e32 v84, 16, v85
	v_and_b32_e32 v85, 0xffff0000, v85
	v_lshlrev_b32_e32 v140, 16, v86
	v_and_b32_e32 v141, 0xffff0000, v86
	v_pk_mul_f32 v[128:129], v[44:45], v[134:135] op_sel_hi:[0,1]
	v_pk_mul_f32 v[134:135], v[44:45], v[136:137] op_sel_hi:[0,1]
	v_pk_mul_f32 v[0:1], v[44:45], v[0:1] op_sel_hi:[0,1]
	v_pk_fma_f32 v[38:39], v[38:39], s[14:15], v[48:49] op_sel_hi:[1,0,1]
	v_pk_fma_f32 v[42:43], v[42:43], s[14:15], v[66:67] op_sel_hi:[1,0,1]
	v_pk_add_f32 v[48:49], v[36:37], v[96:97]
	v_pk_add_f32 v[36:37], v[40:41], v[28:29]
	v_pk_mul_f32 v[28:29], v[44:45], v[144:145] op_sel_hi:[0,1]
	v_lshlrev_b32_e32 v86, 16, v87
	v_and_b32_e32 v87, 0xffff0000, v87
	v_pk_fma_f32 v[64:65], v[4:5], v[130:131], v[128:129] op_sel_hi:[0,1,1]
	v_pk_fma_f32 v[68:69], v[4:5], v[132:133], v[134:135] op_sel_hi:[0,1,1]
	v_pk_add_f32 v[40:41], v[42:43], v[30:31]
	v_pk_fma_f32 v[0:1], v[4:5], v[84:85], v[0:1] op_sel_hi:[0,1,1]
	v_pk_mul_f32 v[30:31], v[44:45], v[146:147] op_sel_hi:[0,1]
	v_pk_fma_f32 v[28:29], v[4:5], v[140:141], v[28:29] op_sel_hi:[0,1,1]
	v_pk_fma_f32 v[64:65], v[118:119], s[14:15], v[64:65] op_sel_hi:[1,0,1]
	v_pk_fma_f32 v[68:69], v[120:121], s[14:15], v[68:69] op_sel_hi:[1,0,1]
	v_pk_fma_f32 v[0:1], v[46:47], s[14:15], v[0:1] op_sel_hi:[1,0,1]
	v_pk_fma_f32 v[30:31], v[4:5], v[86:87], v[30:31] op_sel_hi:[0,1,1]
	v_pk_fma_f32 v[46:47], v[124:125], s[14:15], v[28:29] op_sel_hi:[1,0,1]
	v_pk_fma_f32 v[70:71], v[116:117], s[14:15], v[52:53] op_sel_hi:[1,0,1]
	v_pk_add_f32 v[52:53], v[38:39], v[100:101]
	v_pk_add_f32 v[38:39], v[64:65], v[102:103]
	v_pk_add_f32 v[42:43], v[68:69], v[104:105]
	v_pk_fma_f32 v[28:29], v[126:127], s[14:15], v[30:31] op_sel_hi:[1,0,1]
	v_pk_add_f32 v[30:31], v[46:47], v[110:111]
	v_lshlrev_b32_e32 v46, 16, v80
	v_and_b32_e32 v47, 0xffff0000, v80
	v_lshlrev_b32_e32 v64, 16, v81
	v_and_b32_e32 v65, 0xffff0000, v81
	v_lshlrev_b32_e32 v66, 16, v82
	v_and_b32_e32 v67, 0xffff0000, v82
	v_lshlrev_b32_e32 v68, 16, v83
	v_and_b32_e32 v69, 0xffff0000, v83
	s_waitcnt vmcnt(1)
	v_lshlrev_b32_e32 v80, 16, v34
	v_and_b32_e32 v81, 0xffff0000, v34
	v_lshlrev_b32_e32 v82, 16, v35
	v_and_b32_e32 v83, 0xffff0000, v35
	s_waitcnt vmcnt(0)
	v_lshlrev_b32_e32 v34, 16, v88
	v_and_b32_e32 v35, 0xffff0000, v88
	v_pk_add_f32 v[54:55], v[70:71], v[98:99]
	v_lshlrev_b32_e32 v70, 16, v76
	v_and_b32_e32 v71, 0xffff0000, v76
	v_lshlrev_b32_e32 v72, 16, v77
	v_and_b32_e32 v73, 0xffff0000, v77
	v_lshlrev_b32_e32 v74, 16, v78
	v_and_b32_e32 v75, 0xffff0000, v78
	v_lshlrev_b32_e32 v76, 16, v79
	v_and_b32_e32 v77, 0xffff0000, v79
	v_lshlrev_b32_e32 v78, 16, v32
	v_and_b32_e32 v79, 0xffff0000, v32
	v_pk_mul_f32 v[34:35], v[44:45], v[34:35] op_sel_hi:[0,1]
	v_lshlrev_b32_e32 v84, 16, v89
	v_and_b32_e32 v85, 0xffff0000, v89
	v_lshlrev_b32_e32 v86, 16, v90
	v_and_b32_e32 v87, 0xffff0000, v90
	v_pk_fma_f32 v[34:35], v[4:5], v[78:79], v[34:35] op_sel_hi:[0,1,1]
	v_pk_fma_f32 v[2:3], v[114:115], s[14:15], v[2:3] op_sel_hi:[1,0,1]
	v_lshlrev_b32_e32 v32, 16, v33
	v_and_b32_e32 v33, 0xffff0000, v33
	v_lshlrev_b32_e32 v88, 16, v91
	v_and_b32_e32 v89, 0xffff0000, v91
	v_pk_mul_f32 v[84:85], v[44:45], v[84:85] op_sel_hi:[0,1]
	v_pk_fma_f32 v[34:35], v[46:47], s[14:15], v[34:35] op_sel_hi:[1,0,1]
	v_pk_mul_f32 v[46:47], v[44:45], v[86:87] op_sel_hi:[0,1]
	v_pk_mul_f32 v[136:137], v[44:45], v[142:143] op_sel_hi:[0,1]
	v_pk_add_f32 v[50:51], v[2:3], v[94:95]
	v_pk_fma_f32 v[32:33], v[4:5], v[32:33], v[84:85] op_sel_hi:[0,1,1]
	v_pk_mul_f32 v[44:45], v[44:45], v[88:89] op_sel_hi:[0,1]
	v_pk_fma_f32 v[46:47], v[4:5], v[80:81], v[46:47] op_sel_hi:[0,1,1]
	v_pk_fma_f32 v[32:33], v[64:65], s[14:15], v[32:33] op_sel_hi:[1,0,1]
	v_pk_fma_f32 v[44:45], v[4:5], v[82:83], v[44:45] op_sel_hi:[0,1,1]
	v_pk_fma_f32 v[46:47], v[66:67], s[14:15], v[46:47] op_sel_hi:[1,0,1]
	v_mov_b32_e32 v64, v54
	v_mov_b32_e32 v65, v50
	v_mov_b32_e32 v66, v55
	v_mov_b32_e32 v67, v51
	v_pk_fma_f32 v[44:45], v[68:69], s[14:15], v[44:45] op_sel_hi:[1,0,1]
	v_pk_add_f32 v[64:65], v[64:65], v[66:67]
	v_mov_b32_e32 v66, v52
	v_mov_b32_e32 v67, v48
	v_mov_b32_e32 v68, v53
	v_mov_b32_e32 v69, v49
	v_pk_add_f32 v[66:67], v[66:67], v[68:69]
	v_pk_fma_f32 v[2:3], v[4:5], v[138:139], v[136:137] op_sel_hi:[0,1,1]
	v_pk_add_f32 v[64:65], v[64:65], v[66:67]
; template <bool ROUTE, bool COMBINE> ...
;     ...
;             v[2 * j] = (ALPHA * xa + (g0 * a0 + g1 * c0)) + pa; v[2 * j + 1] = (ALPHA * xb + (g0 * a1 + g1 * c1)) + pb; }
;     }
; #pragma unroll
;     for (int j = 0; j < 8; ++j) s += (v[j].x + v[j].y) + (v[j].z + v[j].w);
;     const float mean = wave_sum(s) * (1.0f / D_); float s2 = 0.f;
; #pragma unroll
;     for (int j = 0; j < 8; ++j) { v[j] = v[j] - mean; s2 += (v[j].x * v[j].x + v[j].y * v[j].y) + (v[j].z * v[j].z + v[j].w * v[j].w); }
;     const float rstd = 1.0f / sqrtf(wave_sum(s2) * (1.0f / D_) + LN_EPS);
	v_pk_mov_b32 v[66:67], v[38:39], v[36:37] op_sel:[1,0]
	v_mov_b32_e32 v68, v38
	v_mov_b32_e32 v69, v37
	v_pk_fma_f32 v[2:3], v[122:123], s[14:15], v[2:3] op_sel_hi:[1,0,1]
	v_pk_add_f32 v[66:67], v[66:67], v[68:69]
	v_pk_add_f32 v[0:1], v[0:1], v[108:109]
	v_pk_add_f32 v[2:3], v[2:3], v[106:107]
	v_add_f32_e32 v4, 0, v65
	v_pk_add_f32 v[66:67], v[66:67], v[66:67] op_sel:[0,1] op_sel_hi:[1,0]
	v_pk_add_f32 v[34:35], v[34:35], v[70:71]
	v_add_f32_e32 v64, v64, v4
	v_add_f32_e32 v68, v42, v43
	v_add_f32_e32 v70, v40, v41
	v_mov_b32_e32 v69, v2
	v_mov_b32_e32 v71, v3
	v_mov_b32_e32 v65, v0
	v_mov_b32_e32 v67, v1
	v_pk_add_f32 v[28:29], v[28:29], v[112:113]
	v_pk_add_f32 v[68:69], v[68:69], v[70:71]
	v_pk_add_f32 v[64:65], v[64:65], v[66:67]
	v_pk_mov_b32 v[66:67], v[30:31], v[28:29] op_sel:[1,0]
	v_pk_add_f32 v[64:65], v[68:69], v[64:65]
	v_mov_b32_e32 v68, v30
	v_mov_b32_e32 v69, v29
	v_pk_add_f32 v[66:67], v[66:67], v[68:69]
	v_pk_add_f32 v[32:33], v[32:33], v[72:73]
	v_pk_add_f32 v[44:45], v[44:45], v[76:77]
	v_pk_add_f32 v[46:47], v[46:47], v[74:75]
	v_pk_add_f32 v[64:65], v[64:65], v[64:65] op_sel_hi:[0,1]
	v_pk_add_f32 v[66:67], v[66:67], v[66:67] op_sel_hi:[0,1]
	v_add_f32_e32 v69, v34, v35
	v_add_f32_e32 v71, v32, v33
	v_mov_b32_e32 v66, v46
	v_mov_b32_e32 v64, v47
	v_mov_b32_e32 v68, v44
	v_mov_b32_e32 v70, v45
	v_pk_add_f32 v[64:65], v[66:67], v[64:65]
	v_pk_add_f32 v[66:67], v[68:69], v[70:71]
	s_nop 0
	v_pk_add_f32 v[64:65], v[64:65], v[66:67]
	s_nop 0
	v_add_f32_e32 v4, v64, v65
	s_nop 1
	v_add_f32_dpp v4, v4, v4 quad_perm:[1,0,3,2] row_mask:0xf bank_mask:0xf
	s_nop 1
	v_add_f32_dpp v4, v4, v4 quad_perm:[2,3,0,1] row_mask:0xf bank_mask:0xf
	s_nop 1
	v_add_f32_dpp v4, v4, v4 row_half_mirror row_mask:0xf bank_mask:0xf
	s_nop 1
	v_add_f32_dpp v4, v4, v4 row_mirror row_mask:0xf bank_mask:0xf
	s_nop 1
	v_add_f32_dpp v4, v4, v4 row_bcast:15 row_mask:0xa bank_mask:0xf
	s_nop 1
	v_add_f32_dpp v4, v4, v4 row_bcast:31 row_mask:0xc bank_mask:0xf
	s_nop 1
	v_readlane_b32 s98, v4, 63
	s_nop 3
	v_mov_b32_e32 v4, s98
	s_waitcnt lgkmcnt(0)
	v_fmamk_f32 v49, v4, 0xba000000, v49
	v_fmamk_f32 v51, v4, 0xba000000, v51
	v_fmac_f32_e32 v48, 0xba000000, v4
	v_fmac_f32_e32 v50, 0xba000000, v4
	v_mul_f32_e32 v64, v51, v51
	v_mul_f32_e32 v65, v49, v49
	v_fmac_f32_e32 v64, v50, v50
	v_fmac_f32_e32 v65, v48, v48
	v_fmamk_f32 v53, v4, 0xba000000, v53
	v_fmamk_f32 v55, v4, 0xba000000, v55
	v_add_f32_e32 v64, v64, v65
	v_fmac_f32_e32 v52, 0xba000000, v4
	v_fmac_f32_e32 v54, 0xba000000, v4
	v_mul_f32_e32 v65, v55, v55
	v_mul_f32_e32 v66, v53, v53
	v_fmac_f32_e32 v65, v54, v54
	v_fmac_f32_e32 v66, v52, v52
	v_add_f32_e32 v65, v65, v66
	v_fmamk_f32 v37, v4, 0xba000000, v37
	v_fmamk_f32 v39, v4, 0xba000000, v39
	v_add_f32_e32 v64, v64, v65
	v_fmac_f32_e32 v36, 0xba000000, v4
	v_fmac_f32_e32 v38, 0xba000000, v4
	v_mul_f32_e32 v65, v39, v39
	v_mul_f32_e32 v66, v37, v37
	v_fmac_f32_e32 v65, v38, v38
	v_fmac_f32_e32 v66, v36, v36
	v_add_f32_e32 v65, v65, v66
	v_fmamk_f32 v41, v4, 0xba000000, v41
	v_fmamk_f32 v43, v4, 0xba000000, v43
	v_add_f32_e32 v64, v65, v64
	v_fmac_f32_e32 v40, 0xba000000, v4
	v_fmac_f32_e32 v42, 0xba000000, v4
	v_mul_f32_e32 v65, v43, v43
	v_mul_f32_e32 v66, v41, v41
	v_fmac_f32_e32 v65, v42, v42
	v_fmac_f32_e32 v66, v40, v40
	v_add_f32_e32 v65, v65, v66
	v_fmamk_f32 v1, v4, 0xba000000, v1
	v_fmamk_f32 v3, v4, 0xba000000, v3
	v_add_f32_e32 v64, v65, v64
	v_fmac_f32_e32 v0, 0xba000000, v4
	v_fmac_f32_e32 v2, 0xba000000, v4
	v_mul_f32_e32 v65, v3, v3
	v_mul_f32_e32 v66, v1, v1
	v_fmac_f32_e32 v65, v2, v2
	v_fmac_f32_e32 v66, v0, v0
	v_add_f32_e32 v65, v65, v66
	v_fmamk_f32 v29, v4, 0xba000000, v29
	v_fmamk_f32 v31, v4, 0xba000000, v31
	v_add_f32_e32 v64, v65, v64
	v_fmac_f32_e32 v28, 0xba000000, v4
	v_fmac_f32_e32 v30, 0xba000000, v4
	v_mul_f32_e32 v65, v31, v31
	v_mul_f32_e32 v66, v29, v29
	v_fmac_f32_e32 v65, v30, v30
	v_fmac_f32_e32 v66, v28, v28
	v_add_f32_e32 v65, v65, v66
	v_fmamk_f32 v33, v4, 0xba000000, v33
	v_fmamk_f32 v35, v4, 0xba000000, v35
	v_add_f32_e32 v64, v65, v64
	v_fmac_f32_e32 v32, 0xba000000, v4
	v_fmac_f32_e32 v34, 0xba000000, v4
	v_mul_f32_e32 v65, v35, v35
	v_mul_f32_e32 v66, v33, v33
	v_fmac_f32_e32 v65, v34, v34
	v_fmac_f32_e32 v66, v32, v32
	v_add_f32_e32 v65, v65, v66
	v_fmamk_f32 v45, v4, 0xba000000, v45
	v_fmamk_f32 v47, v4, 0xba000000, v47
	v_add_f32_e32 v64, v65, v64
	v_fmac_f32_e32 v44, 0xba000000, v4
	v_fmac_f32_e32 v46, 0xba000000, v4
	v_mul_f32_e32 v4, v47, v47
	v_mul_f32_e32 v65, v45, v45
	v_fmac_f32_e32 v4, v46, v46
	v_fmac_f32_e32 v65, v44, v44
	v_add_f32_e32 v4, v4, v65
	v_add_f32_e32 v4, v4, v64
	s_nop 1
	v_add_f32_dpp v4, v4, v4 quad_perm:[1,0,3,2] row_mask:0xf bank_mask:0xf
	s_nop 1
	v_add_f32_dpp v4, v4, v4 quad_perm:[2,3,0,1] row_mask:0xf bank_mask:0xf
	s_nop 1
	v_add_f32_dpp v4, v4, v4 row_half_mirror row_mask:0xf bank_mask:0xf
	s_nop 1
	v_add_f32_dpp v4, v4, v4 row_mirror row_mask:0xf bank_mask:0xf
	s_nop 1
	v_add_f32_dpp v4, v4, v4 row_bcast:15 row_mask:0xa bank_mask:0xf
	s_nop 1
	v_add_f32_dpp v4, v4, v4 row_bcast:31 row_mask:0xc bank_mask:0xf
	s_nop 1
	v_readlane_b32 s98, v4, 63
	s_nop 3
	v_mov_b32_e32 v4, s98
	s_waitcnt lgkmcnt(0)
	s_cbranch_vccnz .LBB0_1774
; template <bool ROUTE, bool COMBINE> ...
;     ...
;     const float rstd = 1.0f / sqrtf(wave_sum(s2) * (1.0f / D_) + LN_EPS);
;     float lg0 = 0.f, lg1 = 0.f, lg2 = 0.f, lg3 = 0.f, lg4 = 0.f, lg5 = 0.f, lg6 = 0.f, lg7 = 0.f;
; #pragma unroll
;     for (int j = 0; j < 4; ++j) {
;         const int c = 8 * lane + 512 * j;
;         const f32x4 oa = v[2 * j] * rstd * *(const f32x4*)(g + c) + *(const f32x4*)(bta + c), ob = v[2 * j + 1] * rstd * *(const f32x4*)(g + c + 4) + *(const f32x4*)(bta + c + 4);
;         if (X) { *(f32x4*)(X + (size_t)row * D_ + c) = oa; *(f32x4*)(X + (size_t)row * D_ + c + 4) = ob; }
	global_load_dwordx4 v[66:69], v[8:9], off offset:16
	global_load_dwordx4 v[70:73], v[6:7], off offset:16
	global_load_dwordx4 v[74:77], v[6:7], off
	global_load_dwordx4 v[78:81], v[8:9], off
	v_fmamk_f32 v4, v4, 0x3a000000, v62
	v_mul_f32_e32 v64, 0x4f800000, v4
	v_cmp_gt_f32_e32 vcc, s22, v4
	s_nop 1
	v_cndmask_b32_e32 v4, v4, v64, vcc
	v_sqrt_f32_e32 v64, v4
	s_nop 0
	v_add_u32_e32 v65, -1, v64
	v_add_u32_e32 v82, 1, v64
	v_fma_f32 v83, -v65, v64, v4
	v_fma_f32 v84, -v82, v64, v4
	v_cmp_ge_f32_e64 s[2:3], 0, v83
	s_nop 1
	v_cndmask_b32_e64 v64, v64, v65, s[2:3]
	v_cmp_lt_f32_e64 s[2:3], 0, v84
	s_nop 1
	v_cndmask_b32_e64 v64, v64, v82, s[2:3]
	v_mul_f32_e32 v65, 0x37800000, v64
	v_cndmask_b32_e32 v64, v64, v65, vcc
	v_cmp_class_f32_e32 vcc, v4, v63
	s_nop 1
	v_cndmask_b32_e32 v4, v64, v4, vcc
	v_div_scale_f32 v64, s[2:3], v4, v4, 1.0
	v_rcp_f32_e32 v65, v64
	v_add_co_u32_e32 v82, vcc, s23, v24
	v_fma_f32 v85, -v64, v65, 1.0
	s_nop 0
	v_addc_co_u32_e32 v83, vcc, -1, v25, vcc
	v_div_scale_f32 v84, vcc, 1.0, v4, 1.0
	v_fmac_f32_e32 v65, v85, v65
	v_mul_f32_e32 v85, v84, v65
	v_fma_f32 v86, -v64, v85, v84
	v_fmac_f32_e32 v85, v86, v65
	v_fma_f32 v64, -v64, v85, v84
	v_div_fmas_f32 v64, v64, v65, v85
	v_div_fixup_f32 v4, v64, v4, 1.0
	v_pk_mul_f32 v[54:55], v[54:55], v[4:5] op_sel_hi:[1,0]
	v_pk_mul_f32 v[52:53], v[52:53], v[4:5] op_sel_hi:[1,0]
	v_pk_mul_f32 v[64:65], v[50:51], v[4:5] op_sel_hi:[1,0]
	v_pk_mul_f32 v[84:85], v[48:49], v[4:5] op_sel_hi:[1,0]
	v_pk_mul_f32 v[42:43], v[42:43], v[4:5] op_sel_hi:[1,0]
	v_pk_mul_f32 v[40:41], v[40:41], v[4:5] op_sel_hi:[1,0]
	v_pk_mul_f32 v[30:31], v[30:31], v[4:5] op_sel_hi:[1,0]
	v_pk_mul_f32 v[28:29], v[28:29], v[4:5] op_sel_hi:[1,0]
	v_pk_mul_f32 v[46:47], v[46:47], v[4:5] op_sel_hi:[1,0]
	v_pk_mul_f32 v[44:45], v[44:45], v[4:5] op_sel_hi:[1,0]
	v_pk_mul_f32 v[34:35], v[34:35], v[4:5] op_sel_hi:[1,0]
	v_pk_mul_f32 v[32:33], v[32:33], v[4:5] op_sel_hi:[1,0]
	s_waitcnt vmcnt(2)
	v_pk_fma_f32 v[50:51], v[52:53], v[72:73], v[68:69]
	v_pk_fma_f32 v[48:49], v[54:55], v[70:71], v[66:67]
	s_waitcnt vmcnt(0)
	v_pk_fma_f32 v[54:55], v[84:85], v[76:77], v[80:81]
	v_pk_fma_f32 v[52:53], v[64:65], v[74:75], v[78:79]
	global_store_dwordx4 v[82:83], v[52:55], off offset:-2064
	global_store_dwordx4 v[82:83], v[48:51], off offset:-2048
	global_load_dwordx4 v[48:51], v[12:13], off offset:16
	s_nop 0
	global_load_dwordx4 v[52:55], v[10:11], off offset:16
	global_load_dwordx4 v[64:67], v[10:11], off
	global_load_dwordx4 v[68:71], v[12:13], off
	v_pk_mul_f32 v[72:73], v[38:39], v[4:5] op_sel_hi:[1,0]
	v_pk_mul_f32 v[74:75], v[36:37], v[4:5] op_sel_hi:[1,0]
	s_waitcnt vmcnt(2)
	v_pk_fma_f32 v[38:39], v[40:41], v[54:55], v[50:51]
	v_pk_fma_f32 v[36:37], v[42:43], v[52:53], v[48:49]
	s_waitcnt vmcnt(0)
	v_pk_fma_f32 v[42:43], v[74:75], v[66:67], v[70:71]
	v_pk_fma_f32 v[40:41], v[72:73], v[64:65], v[68:69]
	global_store_dwordx4 v[82:83], v[40:43], off offset:-16
	global_store_dwordx4 v[24:25], v[36:39], off offset:-4096
	global_load_dwordx4 v[36:39], v[16:17], off offset:16
	s_nop 0
	global_load_dwordx4 v[40:43], v[14:15], off offset:16
	global_load_dwordx4 v[48:51], v[14:15], off
	global_load_dwordx4 v[52:55], v[16:17], off
	v_pk_mul_f32 v[64:65], v[2:3], v[4:5] op_sel_hi:[1,0]
	v_pk_mul_f32 v[66:67], v[0:1], v[4:5] op_sel_hi:[1,0]
	s_waitcnt vmcnt(2)
	v_pk_fma_f32 v[2:3], v[28:29], v[42:43], v[38:39]
	v_pk_fma_f32 v[0:1], v[30:31], v[40:41], v[36:37]
	s_waitcnt vmcnt(0)
	v_pk_fma_f32 v[30:31], v[66:67], v[50:51], v[54:55]
	v_pk_fma_f32 v[28:29], v[64:65], v[48:49], v[52:53]
	global_store_dwordx4 v[24:25], v[28:31], off offset:-2064
	global_store_dwordx4 v[24:25], v[0:3], off offset:-2048
	global_load_dwordx4 v[0:3], v[20:21], off offset:16
	s_nop 0
	global_load_dwordx4 v[28:31], v[18:19], off offset:16
	global_load_dwordx4 v[36:39], v[18:19], off
	global_load_dwordx4 v[40:43], v[20:21], off
	s_waitcnt vmcnt(2)
	v_pk_fma_f32 v[2:3], v[44:45], v[30:31], v[2:3]
	v_pk_fma_f32 v[0:1], v[46:47], v[28:29], v[0:1]
	s_waitcnt vmcnt(0)
	v_pk_fma_f32 v[30:31], v[32:33], v[38:39], v[42:43]
	v_pk_fma_f32 v[28:29], v[34:35], v[36:37], v[40:41]
	global_store_dwordx4 v[24:25], v[28:31], off offset:-16
	global_store_dwordx4 v[24:25], v[0:3], off
	s_branch .LBB0_1774

; __global__ void __launch_bounds__(512, 2) mk_fwd(FArgs args) {
	.amdhsa_kernel _Z6mk_fwd5FArgs
		.amdhsa_group_segment_fixed_size 0
		.amdhsa_private_segment_fixed_size 0
		.amdhsa_kernarg_size 456
		.amdhsa_user_sgpr_count 2
		.amdhsa_user_sgpr_dispatch_ptr 0
		.amdhsa_user_sgpr_queue_ptr 0
		.amdhsa_user_sgpr_kernarg_segment_ptr 1
		.amdhsa_user_sgpr_dispatch_id 0
		.amdhsa_user_sgpr_kernarg_preload_length 0
		.amdhsa_user_sgpr_kernarg_preload_offset 0
		.amdhsa_user_sgpr_private_segment_size 0
		.amdhsa_uses_dynamic_stack 0
		.amdhsa_enable_private_segment 0
		.amdhsa_system_sgpr_workgroup_id_x 1
		.amdhsa_system_sgpr_workgroup_id_y 0
		.amdhsa_system_sgpr_workgroup_id_z 0
		.amdhsa_system_sgpr_workgroup_info 0
		.amdhsa_system_vgpr_workitem_id 0
		.amdhsa_next_free_vgpr 255
		.amdhsa_next_free_sgpr 102
		.amdhsa_accum_offset 256
		.amdhsa_reserve_vcc 1
		.amdhsa_float_round_mode_32 0
		.amdhsa_float_round_mode_16_64 0
		.amdhsa_float_denorm_mode_32 3
		.amdhsa_float_denorm_mode_16_64 3
		.amdhsa_dx10_clamp 1
		.amdhsa_ieee_mode 1
		.amdhsa_fp16_overflow 0
		.amdhsa_tg_split 0
		.amdhsa_exception_fp_ieee_invalid_op 0
		.amdhsa_exception_fp_denorm_src 0
		.amdhsa_exception_fp_ieee_div_zero 0
		.amdhsa_exception_fp_ieee_overflow 0
		.amdhsa_exception_fp_ieee_underflow 0
		.amdhsa_exception_fp_ieee_inexact 0
		.amdhsa_exception_int_div_zero 0
	.end_amdhsa_kernel

; __global__ void __launch_bounds__(512, 2) mk_fwd(FArgs args) {
amdhsa.kernels:
  - .agpr_count:     0
    .args:
      - .offset:         0
        .size:           200
        .value_kind:     by_value
      - .offset:         200
        .size:           4
        .value_kind:     hidden_block_count_x
      - .offset:         204
        .size:           4
        .value_kind:     hidden_block_count_y
      - .offset:         208
        .size:           4
        .value_kind:     hidden_block_count_z
      - .offset:         212
        .size:           2
        .value_kind:     hidden_group_size_x
      - .offset:         214
        .size:           2
        .value_kind:     hidden_group_size_y
      - .offset:         216
        .size:           2
        .value_kind:     hidden_group_size_z
      - .offset:         218
        .size:           2
        .value_kind:     hidden_remainder_x
      - .offset:         220
        .size:           2
        .value_kind:     hidden_remainder_y
      - .offset:         222
        .size:           2
        .value_kind:     hidden_remainder_z
      - .offset:         240
        .size:           8
        .value_kind:     hidden_global_offset_x
      - .offset:         248
        .size:           8
        .value_kind:     hidden_global_offset_y
      - .offset:         256
        .size:           8
        .value_kind:     hidden_global_offset_z
      - .offset:         264
        .size:           2
        .value_kind:     hidden_grid_dims
      - .offset:         320
        .size:           4
        .value_kind:     hidden_dynamic_lds_size
    .group_segment_fixed_size: 0
    .kernarg_segment_align: 8
    .kernarg_segment_size: 456
    .language:       OpenCL C
    .language_version:
      - 2
      - 0
    .max_flat_workgroup_size: 512
    .name:           _Z6mk_fwd5FArgs
    .private_segment_fixed_size: 0
    .sgpr_count:     108
    .sgpr_spill_count: 6
    .symbol:         _Z6mk_fwd5FArgs.kd
    .uniform_work_group_size: 1
    .uses_dynamic_stack: false
    .vgpr_count:     255
    .vgpr_spill_count: 0
    .wavefront_size: 64
